# GEMM K-loops: loop-counter SALU moved in front of the loop-back barrier (back-edge rotation), only the branch stays behind it
# speedup vs baseline: 1.0043x; 1.0043x over previous
.LBB0_180:
	ds_read_b128 v[170:173], v163
	ds_read_b128 v[174:177], v163 offset:1024
	ds_read_b128 v[178:181], v163 offset:2048
	ds_read_b128 v[182:185], v163 offset:3072
	ds_read_b128 v[186:189], v164
	ds_read_b128 v[190:193], v164 offset:1024
	ds_read_b128 v[194:197], v164 offset:2048
	ds_read_b128 v[198:201], v164 offset:3072
	s_add_u32 s54, s50, s4
	s_addc_u32 s55, s51, s5
	s_cmpk_eq_i32 s4, 0x1000
	s_cselect_b64 vcc, -1, 0
	s_and_b64 s[52:53], vcc, exec
	s_cselect_b32 s72, 0, s4
	s_cselect_b32 s71, 0, s5
	s_cselect_b32 s52, s47, s54
	s_cselect_b32 s53, s7, s55
	s_add_u32 s54, s18, s72
	v_cndmask_b32_e32 v140, v128, v166, vcc
	v_cndmask_b32_e32 v129, v132, v168, vcc
	v_cndmask_b32_e32 v154, v130, v167, vcc
	v_cndmask_b32_e32 v131, v134, v169, vcc
	s_addc_u32 s55, s19, s71
	v_lshl_add_u64 v[234:235], v[152:153], 0, s[4:5]
	v_lshl_add_u64 v[234:235], v[234:235], 0, s[14:15]
	s_add_i32 m0, s1, 0xc000
	ds_read_b128 v[202:205], v165
	ds_read_b128 v[206:209], v165 offset:1024
	ds_read_b128 v[210:213], v165 offset:2048
	ds_read_b128 v[214:217], v165 offset:3072
	ds_read_b128 v[218:221], v165 offset:4096
	ds_read_b128 v[222:225], v165 offset:5120
	ds_read_b128 v[226:229], v165 offset:6144
	ds_read_b128 v[230:233], v165 offset:7168
	global_load_lds_dwordx4 v[234:235], off
	v_lshl_add_u64 v[234:235], v[150:151], 0, s[4:5]
	v_lshl_add_u64 v[234:235], v[234:235], 0, s[14:15]
	s_add_i32 m0, s1, 0xe000
	s_nop 0
	global_load_lds_dwordx4 v[234:235], off
	s_waitcnt vmcnt(8)
	s_waitcnt lgkmcnt(0)
	s_barrier
	s_setprio 1
	s_waitcnt lgkmcnt(0)
	v_mfma_f32_16x16x32_bf16 v[60:63], v[170:173], v[202:205], v[60:63]
	v_mfma_f32_16x16x32_bf16 v[56:59], v[178:181], v[202:205], v[56:59]
	v_mfma_f32_16x16x32_bf16 v[52:55], v[170:173], v[210:213], v[52:55]
	v_mfma_f32_16x16x32_bf16 v[48:51], v[178:181], v[210:213], v[48:51]
	v_mfma_f32_16x16x32_bf16 v[44:47], v[170:173], v[218:221], v[44:47]
	v_mfma_f32_16x16x32_bf16 v[40:43], v[178:181], v[218:221], v[40:43]
	v_mfma_f32_16x16x32_bf16 v[36:39], v[170:173], v[226:229], v[36:39]
	v_mfma_f32_16x16x32_bf16 v[32:35], v[178:181], v[226:229], v[32:35]
	v_mfma_f32_16x16x32_bf16 v[60:63], v[174:177], v[206:209], v[60:63]
	v_mfma_f32_16x16x32_bf16 v[56:59], v[182:185], v[206:209], v[56:59]
	v_mfma_f32_16x16x32_bf16 v[52:55], v[174:177], v[214:217], v[52:55]
	v_mfma_f32_16x16x32_bf16 v[48:51], v[182:185], v[214:217], v[48:51]
	v_mfma_f32_16x16x32_bf16 v[44:47], v[174:177], v[222:225], v[44:47]
	v_mfma_f32_16x16x32_bf16 v[40:43], v[182:185], v[222:225], v[40:43]
	v_mfma_f32_16x16x32_bf16 v[36:39], v[174:177], v[230:233], v[36:39]
	v_mfma_f32_16x16x32_bf16 v[32:35], v[182:185], v[230:233], v[32:35]
	s_setprio 0
	s_setprio 1
	v_mfma_f32_16x16x32_bf16 v[124:127], v[186:189], v[202:205], v[124:127]
	v_mfma_f32_16x16x32_bf16 v[120:123], v[194:197], v[202:205], v[120:123]
	v_mfma_f32_16x16x32_bf16 v[116:119], v[186:189], v[210:213], v[116:119]
	v_mfma_f32_16x16x32_bf16 v[112:115], v[194:197], v[210:213], v[112:115]
	v_mfma_f32_16x16x32_bf16 v[108:111], v[186:189], v[218:221], v[108:111]
	v_mfma_f32_16x16x32_bf16 v[104:107], v[194:197], v[218:221], v[104:107]
	v_mfma_f32_16x16x32_bf16 v[100:103], v[186:189], v[226:229], v[100:103]
	v_mfma_f32_16x16x32_bf16 v[96:99], v[194:197], v[226:229], v[96:99]
	v_mfma_f32_16x16x32_bf16 v[124:127], v[190:193], v[206:209], v[124:127]
	v_mfma_f32_16x16x32_bf16 v[120:123], v[198:201], v[206:209], v[120:123]
	v_mfma_f32_16x16x32_bf16 v[116:119], v[190:193], v[214:217], v[116:119]
	v_mfma_f32_16x16x32_bf16 v[112:115], v[198:201], v[214:217], v[112:115]
	v_mfma_f32_16x16x32_bf16 v[108:111], v[190:193], v[222:225], v[108:111]
	v_mfma_f32_16x16x32_bf16 v[104:107], v[198:201], v[222:225], v[104:107]
	v_mfma_f32_16x16x32_bf16 v[100:103], v[190:193], v[230:233], v[100:103]
	v_mfma_f32_16x16x32_bf16 v[96:99], v[198:201], v[230:233], v[96:99]
	s_setprio 0
	s_barrier
	s_add_i32 s71, s66, s0
	v_lshl_add_u64 v[234:235], s[52:53], 0, v[136:137]
	s_mov_b32 m0, s71
	ds_read_b128 v[202:205], v165 offset:16384
	ds_read_b128 v[206:209], v165 offset:17408
	ds_read_b128 v[210:213], v165 offset:18432
	ds_read_b128 v[214:217], v165 offset:19456
	ds_read_b128 v[218:221], v165 offset:20480
	ds_read_b128 v[222:225], v165 offset:21504
	ds_read_b128 v[226:229], v165 offset:22528
	ds_read_b128 v[230:233], v165 offset:23552
	global_load_lds_dwordx4 v[234:235], off
	s_add_i32 m0, s71, 0x2000
	s_add_u32 s72, s52, 0x80000
	v_lshl_add_u64 v[236:237], s[52:53], 0, v[138:139]
	s_addc_u32 s73, s53, 0
	s_add_i32 s71, s67, s0
	global_load_lds_dwordx4 v[236:237], off
	v_lshl_add_u64 v[238:239], s[72:73], 0, v[136:137]
	s_mov_b32 m0, s71
	v_mov_b32_e32 v155, v141
	global_load_lds_dwordx4 v[238:239], off
	v_lshl_add_u64 v[238:239], s[72:73], 0, v[138:139]
	s_add_i32 m0, s71, 0x2000
	s_nop 0
	global_load_lds_dwordx4 v[238:239], off
	s_mov_b32 m0, s1
	v_lshl_add_u64 v[238:239], s[54:55], 0, v[140:141]
	global_load_lds_dwordx4 v140, s[54:55]
	s_mov_b32 m0, s8
	s_nop 0
	global_load_lds_dwordx4 v154, s[54:55]
	s_waitcnt vmcnt(8)
	s_waitcnt lgkmcnt(0)
	v_lshl_add_u64 v[154:155], s[54:55], 0, v[154:155]
	s_barrier
	s_setprio 1
	s_waitcnt lgkmcnt(0)
	v_mfma_f32_16x16x32_bf16 v[28:31], v[170:173], v[202:205], v[28:31]
	v_mfma_f32_16x16x32_bf16 v[24:27], v[178:181], v[202:205], v[24:27]
	v_mfma_f32_16x16x32_bf16 v[20:23], v[170:173], v[210:213], v[20:23]
	v_mfma_f32_16x16x32_bf16 v[16:19], v[178:181], v[210:213], v[16:19]
	v_mfma_f32_16x16x32_bf16 v[12:15], v[170:173], v[218:221], v[12:15]
	v_mfma_f32_16x16x32_bf16 v[8:11], v[178:181], v[218:221], v[8:11]
	v_mfma_f32_16x16x32_bf16 v[4:7], v[170:173], v[226:229], v[4:7]
	v_mfma_f32_16x16x32_bf16 v[0:3], v[178:181], v[226:229], v[0:3]
	v_mfma_f32_16x16x32_bf16 v[28:31], v[174:177], v[206:209], v[28:31]
	v_mfma_f32_16x16x32_bf16 v[24:27], v[182:185], v[206:209], v[24:27]
	v_mfma_f32_16x16x32_bf16 v[20:23], v[174:177], v[214:217], v[20:23]
	v_mfma_f32_16x16x32_bf16 v[16:19], v[182:185], v[214:217], v[16:19]
	v_mfma_f32_16x16x32_bf16 v[12:15], v[174:177], v[222:225], v[12:15]
	v_mfma_f32_16x16x32_bf16 v[8:11], v[182:185], v[222:225], v[8:11]
	v_mfma_f32_16x16x32_bf16 v[4:7], v[174:177], v[230:233], v[4:7]
	v_mfma_f32_16x16x32_bf16 v[0:3], v[182:185], v[230:233], v[0:3]
	s_setprio 0
	s_setprio 1
	v_mfma_f32_16x16x32_bf16 v[92:95], v[186:189], v[202:205], v[92:95]
	v_mfma_f32_16x16x32_bf16 v[88:91], v[194:197], v[202:205], v[88:91]
	v_mfma_f32_16x16x32_bf16 v[84:87], v[186:189], v[210:213], v[84:87]
	v_mfma_f32_16x16x32_bf16 v[80:83], v[194:197], v[210:213], v[80:83]
	v_mfma_f32_16x16x32_bf16 v[72:75], v[186:189], v[218:221], v[72:75]
	v_mfma_f32_16x16x32_bf16 v[76:79], v[194:197], v[218:221], v[76:79]
	v_mfma_f32_16x16x32_bf16 v[64:67], v[186:189], v[226:229], v[64:67]
	v_mfma_f32_16x16x32_bf16 v[68:71], v[194:197], v[226:229], v[68:71]
	v_mfma_f32_16x16x32_bf16 v[92:95], v[190:193], v[206:209], v[92:95]
	v_mfma_f32_16x16x32_bf16 v[88:91], v[198:201], v[206:209], v[88:91]
	v_mfma_f32_16x16x32_bf16 v[84:87], v[190:193], v[214:217], v[84:87]
	v_mfma_f32_16x16x32_bf16 v[80:83], v[198:201], v[214:217], v[80:83]
	v_mfma_f32_16x16x32_bf16 v[72:75], v[190:193], v[222:225], v[72:75]
	v_mfma_f32_16x16x32_bf16 v[76:79], v[198:201], v[222:225], v[76:79]
	v_mfma_f32_16x16x32_bf16 v[64:67], v[190:193], v[230:233], v[64:67]
	v_mfma_f32_16x16x32_bf16 v[68:71], v[198:201], v[230:233], v[68:71]
	s_setprio 0
	s_barrier
	s_add_i32 s71, 0, 0x18000
	v_add_u32_e32 v133, s71, v161
	s_add_i32 s72, 0, 0x1c000
	ds_read_b128 v[170:173], v133
	ds_read_b128 v[174:177], v133 offset:1024
	ds_read_b128 v[178:181], v133 offset:2048
	ds_read_b128 v[182:185], v133 offset:3072
	v_add_u32_e32 v133, s72, v161
	ds_read_b128 v[186:189], v133
	ds_read_b128 v[190:193], v133 offset:1024
	ds_read_b128 v[194:197], v133 offset:2048
	ds_read_b128 v[198:201], v133 offset:3072
	s_mov_b32 m0, s9
	ds_read_b128 v[202:205], v165 offset:32768
	ds_read_b128 v[206:209], v165 offset:33792
	ds_read_b128 v[210:213], v165 offset:34816
	ds_read_b128 v[214:217], v165 offset:35840
	ds_read_b128 v[218:221], v165 offset:36864
	ds_read_b128 v[222:225], v165 offset:37888
	ds_read_b128 v[226:229], v165 offset:38912
	ds_read_b128 v[230:233], v165 offset:39936
	global_load_lds_dwordx4 v129, s[54:55]
	s_mov_b32 m0, s31
	s_nop 0
	global_load_lds_dwordx4 v131, s[54:55]
	s_waitcnt vmcnt(8)
	s_waitcnt lgkmcnt(0)
	s_barrier
	s_setprio 1
	s_waitcnt lgkmcnt(0)
	v_mfma_f32_16x16x32_bf16 v[60:63], v[170:173], v[202:205], v[60:63]
	v_mfma_f32_16x16x32_bf16 v[56:59], v[178:181], v[202:205], v[56:59]
	v_mfma_f32_16x16x32_bf16 v[52:55], v[170:173], v[210:213], v[52:55]
	v_mfma_f32_16x16x32_bf16 v[48:51], v[178:181], v[210:213], v[48:51]
	v_mfma_f32_16x16x32_bf16 v[44:47], v[170:173], v[218:221], v[44:47]
	v_mfma_f32_16x16x32_bf16 v[40:43], v[178:181], v[218:221], v[40:43]
	v_mfma_f32_16x16x32_bf16 v[36:39], v[170:173], v[226:229], v[36:39]
	v_mfma_f32_16x16x32_bf16 v[32:35], v[178:181], v[226:229], v[32:35]
	v_mfma_f32_16x16x32_bf16 v[60:63], v[174:177], v[206:209], v[60:63]
	v_mfma_f32_16x16x32_bf16 v[56:59], v[182:185], v[206:209], v[56:59]
	v_mfma_f32_16x16x32_bf16 v[52:55], v[174:177], v[214:217], v[52:55]
	v_mfma_f32_16x16x32_bf16 v[48:51], v[182:185], v[214:217], v[48:51]
	v_mfma_f32_16x16x32_bf16 v[44:47], v[174:177], v[222:225], v[44:47]
	v_mfma_f32_16x16x32_bf16 v[40:43], v[182:185], v[222:225], v[40:43]
	v_mfma_f32_16x16x32_bf16 v[36:39], v[174:177], v[230:233], v[36:39]
	v_mfma_f32_16x16x32_bf16 v[32:35], v[182:185], v[230:233], v[32:35]
	s_setprio 0
	s_setprio 1
	v_mfma_f32_16x16x32_bf16 v[124:127], v[186:189], v[202:205], v[124:127]
	v_mfma_f32_16x16x32_bf16 v[120:123], v[194:197], v[202:205], v[120:123]
	v_mfma_f32_16x16x32_bf16 v[116:119], v[186:189], v[210:213], v[116:119]
	v_mfma_f32_16x16x32_bf16 v[112:115], v[194:197], v[210:213], v[112:115]
	v_mfma_f32_16x16x32_bf16 v[108:111], v[186:189], v[218:221], v[108:111]
	v_mfma_f32_16x16x32_bf16 v[104:107], v[194:197], v[218:221], v[104:107]
	v_mfma_f32_16x16x32_bf16 v[100:103], v[186:189], v[226:229], v[100:103]
	v_mfma_f32_16x16x32_bf16 v[96:99], v[194:197], v[226:229], v[96:99]
	v_mfma_f32_16x16x32_bf16 v[124:127], v[190:193], v[206:209], v[124:127]
	v_mfma_f32_16x16x32_bf16 v[120:123], v[198:201], v[206:209], v[120:123]
	v_mfma_f32_16x16x32_bf16 v[116:119], v[190:193], v[214:217], v[116:119]
	v_mfma_f32_16x16x32_bf16 v[112:115], v[198:201], v[214:217], v[112:115]
	v_mfma_f32_16x16x32_bf16 v[108:111], v[190:193], v[222:225], v[108:111]
	v_mfma_f32_16x16x32_bf16 v[104:107], v[198:201], v[222:225], v[104:107]
	v_mfma_f32_16x16x32_bf16 v[100:103], v[190:193], v[230:233], v[100:103]
	v_mfma_f32_16x16x32_bf16 v[96:99], v[198:201], v[230:233], v[96:99]
	s_setprio 0
	s_barrier
	s_add_i32 s54, s71, s0
	v_lshl_add_u64 v[234:235], v[234:235], 0, s[24:25]
	s_mov_b32 m0, s54
	ds_read_b128 v[202:205], v165 offset:49152
	ds_read_b128 v[206:209], v165 offset:50176
	ds_read_b128 v[210:213], v165 offset:51200
	ds_read_b128 v[214:217], v165 offset:52224
	ds_read_b128 v[218:221], v165 offset:53248
	ds_read_b128 v[222:225], v165 offset:54272
	ds_read_b128 v[226:229], v165 offset:55296
	ds_read_b128 v[230:233], v165 offset:56320
	global_load_lds_dwordx4 v[234:235], off
	s_add_i32 m0, s54, 0x2000
	s_add_u32 s52, s52, 0x80080
	v_lshl_add_u64 v[234:235], v[236:237], 0, s[24:25]
	s_addc_u32 s53, s53, 0
	s_add_i32 s54, s72, s0
	global_load_lds_dwordx4 v[234:235], off
	v_lshl_add_u64 v[234:235], s[52:53], 0, v[136:137]
	s_mov_b32 m0, s54
	v_lshl_add_u64 v[154:155], v[154:155], 0, s[24:25]
	global_load_lds_dwordx4 v[234:235], off
	v_lshl_add_u64 v[234:235], s[52:53], 0, v[138:139]
	s_add_i32 m0, s54, 0x2000
	s_nop 0
	global_load_lds_dwordx4 v[234:235], off
	v_lshl_add_u64 v[234:235], v[238:239], 0, s[24:25]
	s_mov_b32 m0, s60
	s_nop 0
	global_load_lds_dwordx4 v[234:235], off
	s_mov_b32 m0, s61
	s_nop 0
	global_load_lds_dwordx4 v[154:155], off
	s_waitcnt vmcnt(8)
	s_waitcnt lgkmcnt(0)
	s_barrier
	s_setprio 1
	s_waitcnt lgkmcnt(0)
	v_mfma_f32_16x16x32_bf16 v[28:31], v[170:173], v[202:205], v[28:31]
	v_mfma_f32_16x16x32_bf16 v[24:27], v[178:181], v[202:205], v[24:27]
	v_mfma_f32_16x16x32_bf16 v[20:23], v[170:173], v[210:213], v[20:23]
	v_mfma_f32_16x16x32_bf16 v[16:19], v[178:181], v[210:213], v[16:19]
	v_mfma_f32_16x16x32_bf16 v[12:15], v[170:173], v[218:221], v[12:15]
	v_mfma_f32_16x16x32_bf16 v[8:11], v[178:181], v[218:221], v[8:11]
	v_mfma_f32_16x16x32_bf16 v[4:7], v[170:173], v[226:229], v[4:7]
	v_mfma_f32_16x16x32_bf16 v[0:3], v[178:181], v[226:229], v[0:3]
	v_mfma_f32_16x16x32_bf16 v[28:31], v[174:177], v[206:209], v[28:31]
	v_mfma_f32_16x16x32_bf16 v[24:27], v[182:185], v[206:209], v[24:27]
	v_mfma_f32_16x16x32_bf16 v[20:23], v[174:177], v[214:217], v[20:23]
	v_mfma_f32_16x16x32_bf16 v[16:19], v[182:185], v[214:217], v[16:19]
	v_mfma_f32_16x16x32_bf16 v[12:15], v[174:177], v[222:225], v[12:15]
	v_mfma_f32_16x16x32_bf16 v[8:11], v[182:185], v[222:225], v[8:11]
	v_mfma_f32_16x16x32_bf16 v[4:7], v[174:177], v[230:233], v[4:7]
	v_mfma_f32_16x16x32_bf16 v[0:3], v[182:185], v[230:233], v[0:3]
	s_setprio 0
	s_setprio 1
	v_mfma_f32_16x16x32_bf16 v[92:95], v[186:189], v[202:205], v[92:95]
	v_mfma_f32_16x16x32_bf16 v[88:91], v[194:197], v[202:205], v[88:91]
	v_mfma_f32_16x16x32_bf16 v[84:87], v[186:189], v[210:213], v[84:87]
	v_mfma_f32_16x16x32_bf16 v[80:83], v[194:197], v[210:213], v[80:83]
	v_mfma_f32_16x16x32_bf16 v[72:75], v[186:189], v[218:221], v[72:75]
	v_mfma_f32_16x16x32_bf16 v[76:79], v[194:197], v[218:221], v[76:79]
	v_mfma_f32_16x16x32_bf16 v[64:67], v[186:189], v[226:229], v[64:67]
	v_mfma_f32_16x16x32_bf16 v[68:71], v[194:197], v[226:229], v[68:71]
	v_mfma_f32_16x16x32_bf16 v[92:95], v[190:193], v[206:209], v[92:95]
	v_mfma_f32_16x16x32_bf16 v[88:91], v[198:201], v[206:209], v[88:91]
	v_mfma_f32_16x16x32_bf16 v[84:87], v[190:193], v[214:217], v[84:87]
	v_mfma_f32_16x16x32_bf16 v[80:83], v[198:201], v[214:217], v[80:83]
	v_mfma_f32_16x16x32_bf16 v[72:75], v[190:193], v[222:225], v[72:75]
	v_mfma_f32_16x16x32_bf16 v[76:79], v[198:201], v[222:225], v[76:79]
	v_mfma_f32_16x16x32_bf16 v[64:67], v[190:193], v[230:233], v[64:67]
	v_mfma_f32_16x16x32_bf16 v[68:71], v[198:201], v[230:233], v[68:71]
	s_setprio 0
	s_add_i32 s70, s70, 2
	s_add_u32 s4, s4, 0x100
	s_addc_u32 s5, s5, 0
	s_cmp_gt_u32 s70, 29
	s_barrier
	s_cbranch_scc0 .LBB0_180
	s_and_b64 vcc, exec, s[26:27]
	s_cbranch_vccnz .LBB0_184
	v_lshl_add_u32 v150, s62, 8, v160
	s_cmp_lg_u32 s6, 46
	s_mov_b64 s[4:5], -1
	s_cbranch_scc1 .LBB0_185

.LBB0_888:
	s_add_i32 s63, s38, 2
	s_add_u32 s39, s30, s36
	s_addc_u32 s40, s31, s37
	v_add_u32_e32 v131, s44, v152
	s_add_u32 s64, s39, 0x100
	ds_read_b128 v[160:163], v131
	ds_read_b128 v[164:167], v131 offset:1024
	ds_read_b128 v[168:171], v131 offset:2048
	ds_read_b128 v[172:175], v131 offset:3072
	v_add_u32_e32 v131, s45, v152
	s_addc_u32 s40, s40, 0
	ds_read_b128 v[176:179], v131
	ds_read_b128 v[180:183], v131 offset:1024
	ds_read_b128 v[184:187], v131 offset:2048
	ds_read_b128 v[188:191], v131 offset:3072
	s_add_u32 s65, s61, s36
	s_addc_u32 s66, s62, s37
	s_cmp_eq_u32 s60, s38
	s_cselect_b64 vcc, -1, 0
	s_and_b64 s[38:39], vcc, exec
	s_cselect_b32 s38, s55, s65
	v_cndmask_b32_e32 v136, v128, v156, vcc
	s_cselect_b32 s41, s57, s40
	s_cselect_b32 s40, s59, s64
	v_cndmask_b32_e32 v129, v138, v158, vcc
	v_cndmask_b32_e32 v224, v130, v157, vcc
	v_cndmask_b32_e32 v131, v140, v159, vcc
	s_cselect_b32 s39, s25, s66
	v_lshl_add_u64 v[226:227], v[146:147], 0, s[36:37]
	s_add_i32 m0, s1, 0xc000
	ds_read_b128 v[192:195], v155
	ds_read_b128 v[196:199], v155 offset:1024
	ds_read_b128 v[200:203], v155 offset:2048
	ds_read_b128 v[204:207], v155 offset:3072
	ds_read_b128 v[208:211], v155 offset:4096
	ds_read_b128 v[212:215], v155 offset:5120
	ds_read_b128 v[216:219], v155 offset:6144
	ds_read_b128 v[220:223], v155 offset:7168
	global_load_lds_dwordx4 v[226:227], off
	v_lshl_add_u64 v[226:227], v[142:143], 0, s[36:37]
	s_add_i32 m0, s1, 0xe000
	s_nop 0
	global_load_lds_dwordx4 v[226:227], off
	s_waitcnt vmcnt(8)
	s_waitcnt lgkmcnt(0)
	s_barrier
	s_setprio 1
	s_waitcnt lgkmcnt(0)
	v_mfma_f32_16x16x32_bf16 v[108:111], v[160:163], v[192:195], v[108:111]
	v_mfma_f32_16x16x32_bf16 v[104:107], v[168:171], v[192:195], v[104:107]
	v_mfma_f32_16x16x32_bf16 v[100:103], v[160:163], v[200:203], v[100:103]
	v_mfma_f32_16x16x32_bf16 v[96:99], v[168:171], v[200:203], v[96:99]
	v_mfma_f32_16x16x32_bf16 v[92:95], v[160:163], v[208:211], v[92:95]
	v_mfma_f32_16x16x32_bf16 v[88:91], v[168:171], v[208:211], v[88:91]
	v_mfma_f32_16x16x32_bf16 v[84:87], v[160:163], v[216:219], v[84:87]
	v_mfma_f32_16x16x32_bf16 v[80:83], v[168:171], v[216:219], v[80:83]
	v_mfma_f32_16x16x32_bf16 v[108:111], v[164:167], v[196:199], v[108:111]
	v_mfma_f32_16x16x32_bf16 v[104:107], v[172:175], v[196:199], v[104:107]
	v_mfma_f32_16x16x32_bf16 v[100:103], v[164:167], v[204:207], v[100:103]
	v_mfma_f32_16x16x32_bf16 v[96:99], v[172:175], v[204:207], v[96:99]
	v_mfma_f32_16x16x32_bf16 v[92:95], v[164:167], v[212:215], v[92:95]
	v_mfma_f32_16x16x32_bf16 v[88:91], v[172:175], v[212:215], v[88:91]
	v_mfma_f32_16x16x32_bf16 v[84:87], v[164:167], v[220:223], v[84:87]
	v_mfma_f32_16x16x32_bf16 v[80:83], v[172:175], v[220:223], v[80:83]
	s_setprio 0
	s_setprio 1
	v_mfma_f32_16x16x32_bf16 v[76:79], v[176:179], v[192:195], v[76:79]
	v_mfma_f32_16x16x32_bf16 v[72:75], v[184:187], v[192:195], v[72:75]
	v_mfma_f32_16x16x32_bf16 v[68:71], v[176:179], v[200:203], v[68:71]
	v_mfma_f32_16x16x32_bf16 v[64:67], v[184:187], v[200:203], v[64:67]
	v_mfma_f32_16x16x32_bf16 v[60:63], v[176:179], v[208:211], v[60:63]
	v_mfma_f32_16x16x32_bf16 v[56:59], v[184:187], v[208:211], v[56:59]
	v_mfma_f32_16x16x32_bf16 v[52:55], v[176:179], v[216:219], v[52:55]
	v_mfma_f32_16x16x32_bf16 v[48:51], v[184:187], v[216:219], v[48:51]
	v_mfma_f32_16x16x32_bf16 v[76:79], v[180:183], v[196:199], v[76:79]
	v_mfma_f32_16x16x32_bf16 v[72:75], v[188:191], v[196:199], v[72:75]
	v_mfma_f32_16x16x32_bf16 v[68:71], v[180:183], v[204:207], v[68:71]
	v_mfma_f32_16x16x32_bf16 v[64:67], v[188:191], v[204:207], v[64:67]
	v_mfma_f32_16x16x32_bf16 v[60:63], v[180:183], v[212:215], v[60:63]
	v_mfma_f32_16x16x32_bf16 v[56:59], v[188:191], v[212:215], v[56:59]
	v_mfma_f32_16x16x32_bf16 v[52:55], v[180:183], v[220:223], v[52:55]
	v_mfma_f32_16x16x32_bf16 v[48:51], v[188:191], v[220:223], v[48:51]
	s_setprio 0
	s_barrier
	s_add_i32 s64, s44, s0
	v_lshl_add_u64 v[226:227], s[38:39], 0, v[132:133]
	s_mov_b32 m0, s64
	ds_read_b128 v[192:195], v155 offset:16384
	ds_read_b128 v[196:199], v155 offset:17408
	ds_read_b128 v[200:203], v155 offset:18432
	ds_read_b128 v[204:207], v155 offset:19456
	ds_read_b128 v[208:211], v155 offset:20480
	ds_read_b128 v[212:215], v155 offset:21504
	ds_read_b128 v[216:219], v155 offset:22528
	ds_read_b128 v[220:223], v155 offset:23552
	global_load_lds_dwordx4 v[226:227], off
	s_add_i32 m0, s64, 0x2000
	s_add_u32 s64, s38, 0x80000
	v_lshl_add_u64 v[228:229], s[38:39], 0, v[134:135]
	s_addc_u32 s65, s39, 0
	s_add_i32 s66, s45, s0
	global_load_lds_dwordx4 v[228:229], off
	v_lshl_add_u64 v[230:231], s[64:65], 0, v[132:133]
	s_mov_b32 m0, s66
	v_mov_b32_e32 v225, v137
	global_load_lds_dwordx4 v[230:231], off
	v_lshl_add_u64 v[230:231], s[64:65], 0, v[134:135]
	s_add_i32 m0, s66, 0x2000
	s_nop 0
	global_load_lds_dwordx4 v[230:231], off
	s_mov_b32 m0, s1
	v_lshl_add_u64 v[230:231], s[40:41], 0, v[136:137]
	global_load_lds_dwordx4 v136, s[40:41]
	s_mov_b32 m0, s4
	s_nop 0
	global_load_lds_dwordx4 v224, s[40:41]
	s_waitcnt vmcnt(8)
	s_waitcnt lgkmcnt(0)
	v_lshl_add_u64 v[224:225], s[40:41], 0, v[224:225]
	s_barrier
	s_setprio 1
	s_waitcnt lgkmcnt(0)
	v_mfma_f32_16x16x32_bf16 v[44:47], v[160:163], v[192:195], v[44:47]
	v_mfma_f32_16x16x32_bf16 v[40:43], v[168:171], v[192:195], v[40:43]
	v_mfma_f32_16x16x32_bf16 v[36:39], v[160:163], v[200:203], v[36:39]
	v_mfma_f32_16x16x32_bf16 v[32:35], v[168:171], v[200:203], v[32:35]
	v_mfma_f32_16x16x32_bf16 v[28:31], v[160:163], v[208:211], v[28:31]
	v_mfma_f32_16x16x32_bf16 v[24:27], v[168:171], v[208:211], v[24:27]
	v_mfma_f32_16x16x32_bf16 v[20:23], v[160:163], v[216:219], v[20:23]
	v_mfma_f32_16x16x32_bf16 v[16:19], v[168:171], v[216:219], v[16:19]
	v_mfma_f32_16x16x32_bf16 v[44:47], v[164:167], v[196:199], v[44:47]
	v_mfma_f32_16x16x32_bf16 v[40:43], v[172:175], v[196:199], v[40:43]
	v_mfma_f32_16x16x32_bf16 v[36:39], v[164:167], v[204:207], v[36:39]
	v_mfma_f32_16x16x32_bf16 v[32:35], v[172:175], v[204:207], v[32:35]
	v_mfma_f32_16x16x32_bf16 v[28:31], v[164:167], v[212:215], v[28:31]
	v_mfma_f32_16x16x32_bf16 v[24:27], v[172:175], v[212:215], v[24:27]
	v_mfma_f32_16x16x32_bf16 v[20:23], v[164:167], v[220:223], v[20:23]
	v_mfma_f32_16x16x32_bf16 v[16:19], v[172:175], v[220:223], v[16:19]
	s_setprio 0
	s_setprio 1
	v_mfma_f32_16x16x32_bf16 v[12:15], v[176:179], v[192:195], v[12:15]
	v_mfma_f32_16x16x32_bf16 v[8:11], v[184:187], v[192:195], v[8:11]
	v_mfma_f32_16x16x32_bf16 v[4:7], v[176:179], v[200:203], v[4:7]
	v_mfma_f32_16x16x32_bf16 v[0:3], v[184:187], v[200:203], v[0:3]
	v_mfma_f32_16x16x32_bf16 v[112:115], v[176:179], v[208:211], v[112:115]
	v_mfma_f32_16x16x32_bf16 v[116:119], v[184:187], v[208:211], v[116:119]
	v_mfma_f32_16x16x32_bf16 v[120:123], v[176:179], v[216:219], v[120:123]
	v_mfma_f32_16x16x32_bf16 v[124:127], v[184:187], v[216:219], v[124:127]
	v_mfma_f32_16x16x32_bf16 v[12:15], v[180:183], v[196:199], v[12:15]
	v_mfma_f32_16x16x32_bf16 v[8:11], v[188:191], v[196:199], v[8:11]
	v_mfma_f32_16x16x32_bf16 v[4:7], v[180:183], v[204:207], v[4:7]
	v_mfma_f32_16x16x32_bf16 v[0:3], v[188:191], v[204:207], v[0:3]
	v_mfma_f32_16x16x32_bf16 v[112:115], v[180:183], v[212:215], v[112:115]
	v_mfma_f32_16x16x32_bf16 v[116:119], v[188:191], v[212:215], v[116:119]
	v_mfma_f32_16x16x32_bf16 v[120:123], v[180:183], v[220:223], v[120:123]
	v_mfma_f32_16x16x32_bf16 v[124:127], v[188:191], v[220:223], v[124:127]
	s_setprio 0
	s_barrier
	s_add_i32 s64, 0, 0x18000
	v_add_u32_e32 v136, s64, v152
	s_add_i32 s65, 0, 0x1c000
	ds_read_b128 v[160:163], v136
	ds_read_b128 v[164:167], v136 offset:1024
	ds_read_b128 v[168:171], v136 offset:2048
	ds_read_b128 v[172:175], v136 offset:3072
	v_add_u32_e32 v136, s65, v152
	ds_read_b128 v[176:179], v136
	ds_read_b128 v[180:183], v136 offset:1024
	ds_read_b128 v[184:187], v136 offset:2048
	ds_read_b128 v[188:191], v136 offset:3072
	s_mov_b32 m0, s5
	ds_read_b128 v[192:195], v155 offset:32768
	ds_read_b128 v[196:199], v155 offset:33792
	ds_read_b128 v[200:203], v155 offset:34816
	ds_read_b128 v[204:207], v155 offset:35840
	ds_read_b128 v[208:211], v155 offset:36864
	ds_read_b128 v[212:215], v155 offset:37888
	ds_read_b128 v[216:219], v155 offset:38912
	ds_read_b128 v[220:223], v155 offset:39936
	global_load_lds_dwordx4 v129, s[40:41]
	s_mov_b32 m0, s6
	s_nop 0
	global_load_lds_dwordx4 v131, s[40:41]
	s_waitcnt vmcnt(8)
	s_waitcnt lgkmcnt(0)
	s_barrier
	s_setprio 1
	s_waitcnt lgkmcnt(0)
	v_mfma_f32_16x16x32_bf16 v[108:111], v[160:163], v[192:195], v[108:111]
	v_mfma_f32_16x16x32_bf16 v[104:107], v[168:171], v[192:195], v[104:107]
	v_mfma_f32_16x16x32_bf16 v[100:103], v[160:163], v[200:203], v[100:103]
	v_mfma_f32_16x16x32_bf16 v[96:99], v[168:171], v[200:203], v[96:99]
	v_mfma_f32_16x16x32_bf16 v[92:95], v[160:163], v[208:211], v[92:95]
	v_mfma_f32_16x16x32_bf16 v[88:91], v[168:171], v[208:211], v[88:91]
	v_mfma_f32_16x16x32_bf16 v[84:87], v[160:163], v[216:219], v[84:87]
	v_mfma_f32_16x16x32_bf16 v[80:83], v[168:171], v[216:219], v[80:83]
	v_mfma_f32_16x16x32_bf16 v[108:111], v[164:167], v[196:199], v[108:111]
	v_mfma_f32_16x16x32_bf16 v[104:107], v[172:175], v[196:199], v[104:107]
	v_mfma_f32_16x16x32_bf16 v[100:103], v[164:167], v[204:207], v[100:103]
	v_mfma_f32_16x16x32_bf16 v[96:99], v[172:175], v[204:207], v[96:99]
	v_mfma_f32_16x16x32_bf16 v[92:95], v[164:167], v[212:215], v[92:95]
	v_mfma_f32_16x16x32_bf16 v[88:91], v[172:175], v[212:215], v[88:91]
	v_mfma_f32_16x16x32_bf16 v[84:87], v[164:167], v[220:223], v[84:87]
	v_mfma_f32_16x16x32_bf16 v[80:83], v[172:175], v[220:223], v[80:83]
	s_setprio 0
	s_setprio 1
	v_mfma_f32_16x16x32_bf16 v[76:79], v[176:179], v[192:195], v[76:79]
	v_mfma_f32_16x16x32_bf16 v[72:75], v[184:187], v[192:195], v[72:75]
	v_mfma_f32_16x16x32_bf16 v[68:71], v[176:179], v[200:203], v[68:71]
	v_mfma_f32_16x16x32_bf16 v[64:67], v[184:187], v[200:203], v[64:67]
	v_mfma_f32_16x16x32_bf16 v[60:63], v[176:179], v[208:211], v[60:63]
	v_mfma_f32_16x16x32_bf16 v[56:59], v[184:187], v[208:211], v[56:59]
	v_mfma_f32_16x16x32_bf16 v[52:55], v[176:179], v[216:219], v[52:55]
	v_mfma_f32_16x16x32_bf16 v[48:51], v[184:187], v[216:219], v[48:51]
	v_mfma_f32_16x16x32_bf16 v[76:79], v[180:183], v[196:199], v[76:79]
	v_mfma_f32_16x16x32_bf16 v[72:75], v[188:191], v[196:199], v[72:75]
	v_mfma_f32_16x16x32_bf16 v[68:71], v[180:183], v[204:207], v[68:71]
	v_mfma_f32_16x16x32_bf16 v[64:67], v[188:191], v[204:207], v[64:67]
	v_mfma_f32_16x16x32_bf16 v[60:63], v[180:183], v[212:215], v[60:63]
	v_mfma_f32_16x16x32_bf16 v[56:59], v[188:191], v[212:215], v[56:59]
	v_mfma_f32_16x16x32_bf16 v[52:55], v[180:183], v[220:223], v[52:55]
	v_mfma_f32_16x16x32_bf16 v[48:51], v[188:191], v[220:223], v[48:51]
	s_setprio 0
	s_barrier
	s_add_i32 s40, s64, s0
	v_lshl_add_u64 v[226:227], v[226:227], 0, s[18:19]
	s_mov_b32 m0, s40
	ds_read_b128 v[192:195], v155 offset:49152
	ds_read_b128 v[196:199], v155 offset:50176
	ds_read_b128 v[200:203], v155 offset:51200
	ds_read_b128 v[204:207], v155 offset:52224
	ds_read_b128 v[208:211], v155 offset:53248
	ds_read_b128 v[212:215], v155 offset:54272
	ds_read_b128 v[216:219], v155 offset:55296
	ds_read_b128 v[220:223], v155 offset:56320
	global_load_lds_dwordx4 v[226:227], off
	s_add_i32 m0, s40, 0x2000
	s_add_u32 s38, s38, 0x80080
	v_lshl_add_u64 v[226:227], v[228:229], 0, s[18:19]
	s_addc_u32 s39, s39, 0
	s_add_i32 s40, s65, s0
	global_load_lds_dwordx4 v[226:227], off
	v_lshl_add_u64 v[226:227], s[38:39], 0, v[132:133]
	s_mov_b32 m0, s40
	v_lshl_add_u64 v[224:225], v[224:225], 0, s[18:19]
	global_load_lds_dwordx4 v[226:227], off
	v_lshl_add_u64 v[226:227], s[38:39], 0, v[134:135]
	s_add_i32 m0, s40, 0x2000
	s_nop 0
	global_load_lds_dwordx4 v[226:227], off
	v_lshl_add_u64 v[226:227], v[230:231], 0, s[18:19]
	s_mov_b32 m0, s9
	s_nop 0
	global_load_lds_dwordx4 v[226:227], off
	s_mov_b32 m0, s42
	s_nop 0
	global_load_lds_dwordx4 v[224:225], off
	s_waitcnt vmcnt(8)
	s_waitcnt lgkmcnt(0)
	s_barrier
	s_setprio 1
	s_waitcnt lgkmcnt(0)
	v_mfma_f32_16x16x32_bf16 v[44:47], v[160:163], v[192:195], v[44:47]
	v_mfma_f32_16x16x32_bf16 v[40:43], v[168:171], v[192:195], v[40:43]
	v_mfma_f32_16x16x32_bf16 v[36:39], v[160:163], v[200:203], v[36:39]
	v_mfma_f32_16x16x32_bf16 v[32:35], v[168:171], v[200:203], v[32:35]
	v_mfma_f32_16x16x32_bf16 v[28:31], v[160:163], v[208:211], v[28:31]
	v_mfma_f32_16x16x32_bf16 v[24:27], v[168:171], v[208:211], v[24:27]
	v_mfma_f32_16x16x32_bf16 v[20:23], v[160:163], v[216:219], v[20:23]
	v_mfma_f32_16x16x32_bf16 v[16:19], v[168:171], v[216:219], v[16:19]
	v_mfma_f32_16x16x32_bf16 v[44:47], v[164:167], v[196:199], v[44:47]
	v_mfma_f32_16x16x32_bf16 v[40:43], v[172:175], v[196:199], v[40:43]
	v_mfma_f32_16x16x32_bf16 v[36:39], v[164:167], v[204:207], v[36:39]
	v_mfma_f32_16x16x32_bf16 v[32:35], v[172:175], v[204:207], v[32:35]
	v_mfma_f32_16x16x32_bf16 v[28:31], v[164:167], v[212:215], v[28:31]
	v_mfma_f32_16x16x32_bf16 v[24:27], v[172:175], v[212:215], v[24:27]
	v_mfma_f32_16x16x32_bf16 v[20:23], v[164:167], v[220:223], v[20:23]
	v_mfma_f32_16x16x32_bf16 v[16:19], v[172:175], v[220:223], v[16:19]
	s_setprio 0
	s_setprio 1
	v_mfma_f32_16x16x32_bf16 v[12:15], v[176:179], v[192:195], v[12:15]
	v_mfma_f32_16x16x32_bf16 v[8:11], v[184:187], v[192:195], v[8:11]
	v_mfma_f32_16x16x32_bf16 v[4:7], v[176:179], v[200:203], v[4:7]
	v_mfma_f32_16x16x32_bf16 v[0:3], v[184:187], v[200:203], v[0:3]
	v_mfma_f32_16x16x32_bf16 v[112:115], v[176:179], v[208:211], v[112:115]
	v_mfma_f32_16x16x32_bf16 v[116:119], v[184:187], v[208:211], v[116:119]
	v_mfma_f32_16x16x32_bf16 v[120:123], v[176:179], v[216:219], v[120:123]
	v_mfma_f32_16x16x32_bf16 v[124:127], v[184:187], v[216:219], v[124:127]
	v_mfma_f32_16x16x32_bf16 v[12:15], v[180:183], v[196:199], v[12:15]
	v_mfma_f32_16x16x32_bf16 v[8:11], v[188:191], v[196:199], v[8:11]
	v_mfma_f32_16x16x32_bf16 v[4:7], v[180:183], v[204:207], v[4:7]
	v_mfma_f32_16x16x32_bf16 v[0:3], v[188:191], v[204:207], v[0:3]
	v_mfma_f32_16x16x32_bf16 v[112:115], v[180:183], v[212:215], v[112:115]
	v_mfma_f32_16x16x32_bf16 v[116:119], v[188:191], v[212:215], v[116:119]
	v_mfma_f32_16x16x32_bf16 v[120:123], v[180:183], v[220:223], v[120:123]
	v_mfma_f32_16x16x32_bf16 v[124:127], v[188:191], v[220:223], v[124:127]
	s_setprio 0
	s_add_u32 s36, s36, 0x100
	s_addc_u32 s37, s37, 0
	s_cmp_ge_i32 s63, s53
	s_mov_b32 s38, s63
	s_barrier
	s_cbranch_scc0 .LBB0_888
	s_and_b64 vcc, exec, s[20:21]
	s_cbranch_vccz .LBB0_891
	s_barrier

.LBB0_964:
	ds_read_b128 v[140:143], v162
	ds_read_b128 v[170:173], v162 offset:1024
	ds_read_b128 v[174:177], v162 offset:2048
	ds_read_b128 v[178:181], v162 offset:3072
	ds_read_b128 v[182:185], v163
	ds_read_b128 v[186:189], v163 offset:1024
	ds_read_b128 v[190:193], v163 offset:2048
	ds_read_b128 v[194:197], v163 offset:3072
	s_add_u32 s46, s42, s12
	s_addc_u32 s47, s43, s13
	s_cmpk_eq_i32 s12, 0x1000
	s_cselect_b64 vcc, -1, 0
	s_and_b64 s[44:45], vcc, exec
	s_cselect_b32 s64, 0, s12
	s_cselect_b32 s63, 0, s13
	s_cselect_b32 s44, s61, s46
	s_cselect_b32 s45, s39, s47
	s_add_u32 s46, s14, s64
	v_cndmask_b32_e32 v150, v128, v165, vcc
	v_cndmask_b32_e32 v129, v132, v167, vcc
	v_cndmask_b32_e32 v230, v130, v166, vcc
	v_cndmask_b32_e32 v131, v134, v168, vcc
	s_addc_u32 s47, s15, s63
	v_lshl_add_u64 v[232:233], v[138:139], 0, s[12:13]
	v_lshl_add_u64 v[232:233], v[232:233], 0, s[28:29]
	s_add_i32 m0, s4, 0xc000
	ds_read_b128 v[198:201], v164
	ds_read_b128 v[202:205], v164 offset:1024
	ds_read_b128 v[206:209], v164 offset:2048
	ds_read_b128 v[210:213], v164 offset:3072
	ds_read_b128 v[214:217], v164 offset:4096
	ds_read_b128 v[218:221], v164 offset:5120
	ds_read_b128 v[222:225], v164 offset:6144
	ds_read_b128 v[226:229], v164 offset:7168
	global_load_lds_dwordx4 v[232:233], off
	v_lshl_add_u64 v[232:233], v[136:137], 0, s[12:13]
	v_lshl_add_u64 v[232:233], v[232:233], 0, s[28:29]
	s_add_i32 m0, s4, 0xe000
	s_nop 0
	global_load_lds_dwordx4 v[232:233], off
	s_waitcnt vmcnt(8)
	s_waitcnt lgkmcnt(0)
	s_barrier
	s_setprio 1
	s_waitcnt lgkmcnt(0)
	v_mfma_f32_16x16x32_bf16 v[124:127], v[140:143], v[198:201], v[124:127]
	v_mfma_f32_16x16x32_bf16 v[120:123], v[174:177], v[198:201], v[120:123]
	v_mfma_f32_16x16x32_bf16 v[116:119], v[140:143], v[206:209], v[116:119]
	v_mfma_f32_16x16x32_bf16 v[112:115], v[174:177], v[206:209], v[112:115]
	v_mfma_f32_16x16x32_bf16 v[108:111], v[140:143], v[214:217], v[108:111]
	v_mfma_f32_16x16x32_bf16 v[100:103], v[174:177], v[214:217], v[100:103]
	v_mfma_f32_16x16x32_bf16 v[92:95], v[140:143], v[222:225], v[92:95]
	v_mfma_f32_16x16x32_bf16 v[84:87], v[174:177], v[222:225], v[84:87]
	v_mfma_f32_16x16x32_bf16 v[124:127], v[170:173], v[202:205], v[124:127]
	v_mfma_f32_16x16x32_bf16 v[120:123], v[178:181], v[202:205], v[120:123]
	v_mfma_f32_16x16x32_bf16 v[116:119], v[170:173], v[210:213], v[116:119]
	v_mfma_f32_16x16x32_bf16 v[112:115], v[178:181], v[210:213], v[112:115]
	v_mfma_f32_16x16x32_bf16 v[108:111], v[170:173], v[218:221], v[108:111]
	v_mfma_f32_16x16x32_bf16 v[100:103], v[178:181], v[218:221], v[100:103]
	v_mfma_f32_16x16x32_bf16 v[92:95], v[170:173], v[226:229], v[92:95]
	v_mfma_f32_16x16x32_bf16 v[84:87], v[178:181], v[226:229], v[84:87]
	s_setprio 0
	s_setprio 1
	v_mfma_f32_16x16x32_bf16 v[104:107], v[182:185], v[198:201], v[104:107]
	v_mfma_f32_16x16x32_bf16 v[96:99], v[190:193], v[198:201], v[96:99]
	v_mfma_f32_16x16x32_bf16 v[88:91], v[182:185], v[206:209], v[88:91]
	v_mfma_f32_16x16x32_bf16 v[80:83], v[190:193], v[206:209], v[80:83]
	v_mfma_f32_16x16x32_bf16 v[76:79], v[182:185], v[214:217], v[76:79]
	v_mfma_f32_16x16x32_bf16 v[72:75], v[190:193], v[214:217], v[72:75]
	v_mfma_f32_16x16x32_bf16 v[68:71], v[182:185], v[222:225], v[68:71]
	v_mfma_f32_16x16x32_bf16 v[64:67], v[190:193], v[222:225], v[64:67]
	v_mfma_f32_16x16x32_bf16 v[104:107], v[186:189], v[202:205], v[104:107]
	v_mfma_f32_16x16x32_bf16 v[96:99], v[194:197], v[202:205], v[96:99]
	v_mfma_f32_16x16x32_bf16 v[88:91], v[186:189], v[210:213], v[88:91]
	v_mfma_f32_16x16x32_bf16 v[80:83], v[194:197], v[210:213], v[80:83]
	v_mfma_f32_16x16x32_bf16 v[76:79], v[186:189], v[218:221], v[76:79]
	v_mfma_f32_16x16x32_bf16 v[72:75], v[194:197], v[218:221], v[72:75]
	v_mfma_f32_16x16x32_bf16 v[68:71], v[186:189], v[226:229], v[68:71]
	v_mfma_f32_16x16x32_bf16 v[64:67], v[194:197], v[226:229], v[64:67]
	s_setprio 0
	s_barrier
	s_add_i32 s63, s50, s1
	v_lshl_add_u64 v[232:233], s[44:45], 0, v[146:147]
	s_mov_b32 m0, s63
	ds_read_b128 v[198:201], v164 offset:16384
	ds_read_b128 v[202:205], v164 offset:17408
	ds_read_b128 v[206:209], v164 offset:18432
	ds_read_b128 v[210:213], v164 offset:19456
	ds_read_b128 v[214:217], v164 offset:20480
	ds_read_b128 v[218:221], v164 offset:21504
	ds_read_b128 v[222:225], v164 offset:22528
	ds_read_b128 v[226:229], v164 offset:23552
	global_load_lds_dwordx4 v[232:233], off
	s_add_i32 m0, s63, 0x2000
	s_add_u32 s64, s44, 0x80000
	v_lshl_add_u64 v[234:235], s[44:45], 0, v[148:149]
	s_addc_u32 s65, s45, 0
	s_add_i32 s63, s51, s1
	global_load_lds_dwordx4 v[234:235], off
	v_lshl_add_u64 v[236:237], s[64:65], 0, v[146:147]
	s_mov_b32 m0, s63
	v_mov_b32_e32 v231, v151
	global_load_lds_dwordx4 v[236:237], off
	v_lshl_add_u64 v[236:237], s[64:65], 0, v[148:149]
	s_add_i32 m0, s63, 0x2000
	s_nop 0
	global_load_lds_dwordx4 v[236:237], off
	s_mov_b32 m0, s4
	v_lshl_add_u64 v[236:237], s[46:47], 0, v[150:151]
	global_load_lds_dwordx4 v150, s[46:47]
	s_mov_b32 m0, s5
	s_nop 0
	global_load_lds_dwordx4 v230, s[46:47]
	s_waitcnt vmcnt(8)
	s_waitcnt lgkmcnt(0)
	v_lshl_add_u64 v[230:231], s[46:47], 0, v[230:231]
	s_barrier
	s_setprio 1
	s_waitcnt lgkmcnt(0)
	v_mfma_f32_16x16x32_bf16 v[60:63], v[140:143], v[198:201], v[60:63]
	v_mfma_f32_16x16x32_bf16 v[56:59], v[174:177], v[198:201], v[56:59]
	v_mfma_f32_16x16x32_bf16 v[44:47], v[140:143], v[206:209], v[44:47]
	v_mfma_f32_16x16x32_bf16 v[36:39], v[174:177], v[206:209], v[36:39]
	v_mfma_f32_16x16x32_bf16 v[20:23], v[140:143], v[214:217], v[20:23]
	v_mfma_f32_16x16x32_bf16 v[12:15], v[174:177], v[214:217], v[12:15]
	v_mfma_f32_16x16x32_bf16 v[4:7], v[140:143], v[222:225], v[4:7]
	v_mfma_f32_16x16x32_bf16 v[0:3], v[174:177], v[222:225], v[0:3]
	v_mfma_f32_16x16x32_bf16 v[60:63], v[170:173], v[202:205], v[60:63]
	v_mfma_f32_16x16x32_bf16 v[56:59], v[178:181], v[202:205], v[56:59]
	v_mfma_f32_16x16x32_bf16 v[44:47], v[170:173], v[210:213], v[44:47]
	v_mfma_f32_16x16x32_bf16 v[36:39], v[178:181], v[210:213], v[36:39]
	v_mfma_f32_16x16x32_bf16 v[20:23], v[170:173], v[218:221], v[20:23]
	v_mfma_f32_16x16x32_bf16 v[12:15], v[178:181], v[218:221], v[12:15]
	v_mfma_f32_16x16x32_bf16 v[4:7], v[170:173], v[226:229], v[4:7]
	v_mfma_f32_16x16x32_bf16 v[0:3], v[178:181], v[226:229], v[0:3]
	s_setprio 0
	s_setprio 1
	v_mfma_f32_16x16x32_bf16 v[40:43], v[182:185], v[198:201], v[40:43]
	v_mfma_f32_16x16x32_bf16 v[32:35], v[190:193], v[198:201], v[32:35]
	v_mfma_f32_16x16x32_bf16 v[16:19], v[182:185], v[206:209], v[16:19]
	v_mfma_f32_16x16x32_bf16 v[8:11], v[190:193], v[206:209], v[8:11]
	v_mfma_f32_16x16x32_bf16 v[48:51], v[182:185], v[214:217], v[48:51]
	v_mfma_f32_16x16x32_bf16 v[52:55], v[190:193], v[214:217], v[52:55]
	v_mfma_f32_16x16x32_bf16 v[24:27], v[182:185], v[222:225], v[24:27]
	v_mfma_f32_16x16x32_bf16 v[28:31], v[190:193], v[222:225], v[28:31]
	v_mfma_f32_16x16x32_bf16 v[40:43], v[186:189], v[202:205], v[40:43]
	v_mfma_f32_16x16x32_bf16 v[32:35], v[194:197], v[202:205], v[32:35]
	v_mfma_f32_16x16x32_bf16 v[16:19], v[186:189], v[210:213], v[16:19]
	v_mfma_f32_16x16x32_bf16 v[8:11], v[194:197], v[210:213], v[8:11]
	v_mfma_f32_16x16x32_bf16 v[48:51], v[186:189], v[218:221], v[48:51]
	v_mfma_f32_16x16x32_bf16 v[52:55], v[194:197], v[218:221], v[52:55]
	v_mfma_f32_16x16x32_bf16 v[24:27], v[186:189], v[226:229], v[24:27]
	v_mfma_f32_16x16x32_bf16 v[28:31], v[194:197], v[226:229], v[28:31]
	s_setprio 0
	s_barrier
	s_add_i32 s63, 0, 0x18000
	v_add_u32_e32 v133, s63, v160
	s_add_i32 s64, 0, 0x1c000
	ds_read_b128 v[140:143], v133
	ds_read_b128 v[170:173], v133 offset:1024
	ds_read_b128 v[174:177], v133 offset:2048
	ds_read_b128 v[178:181], v133 offset:3072
	v_add_u32_e32 v133, s64, v160
	ds_read_b128 v[182:185], v133
	ds_read_b128 v[186:189], v133 offset:1024
	ds_read_b128 v[190:193], v133 offset:2048
	ds_read_b128 v[194:197], v133 offset:3072
	s_mov_b32 m0, s6
	ds_read_b128 v[198:201], v164 offset:32768
	ds_read_b128 v[202:205], v164 offset:33792
	ds_read_b128 v[206:209], v164 offset:34816
	ds_read_b128 v[210:213], v164 offset:35840
	ds_read_b128 v[214:217], v164 offset:36864
	ds_read_b128 v[218:221], v164 offset:37888
	ds_read_b128 v[222:225], v164 offset:38912
	ds_read_b128 v[226:229], v164 offset:39936
	global_load_lds_dwordx4 v129, s[46:47]
	s_mov_b32 m0, s7
	s_nop 0
	global_load_lds_dwordx4 v131, s[46:47]
	s_waitcnt vmcnt(8)
	s_waitcnt lgkmcnt(0)
	s_barrier
	s_setprio 1
	s_waitcnt lgkmcnt(0)
	v_mfma_f32_16x16x32_bf16 v[124:127], v[140:143], v[198:201], v[124:127]
	v_mfma_f32_16x16x32_bf16 v[120:123], v[174:177], v[198:201], v[120:123]
	v_mfma_f32_16x16x32_bf16 v[116:119], v[140:143], v[206:209], v[116:119]
	v_mfma_f32_16x16x32_bf16 v[112:115], v[174:177], v[206:209], v[112:115]
	v_mfma_f32_16x16x32_bf16 v[108:111], v[140:143], v[214:217], v[108:111]
	v_mfma_f32_16x16x32_bf16 v[100:103], v[174:177], v[214:217], v[100:103]
	v_mfma_f32_16x16x32_bf16 v[92:95], v[140:143], v[222:225], v[92:95]
	v_mfma_f32_16x16x32_bf16 v[84:87], v[174:177], v[222:225], v[84:87]
	v_mfma_f32_16x16x32_bf16 v[124:127], v[170:173], v[202:205], v[124:127]
	v_mfma_f32_16x16x32_bf16 v[120:123], v[178:181], v[202:205], v[120:123]
	v_mfma_f32_16x16x32_bf16 v[116:119], v[170:173], v[210:213], v[116:119]
	v_mfma_f32_16x16x32_bf16 v[112:115], v[178:181], v[210:213], v[112:115]
	v_mfma_f32_16x16x32_bf16 v[108:111], v[170:173], v[218:221], v[108:111]
	v_mfma_f32_16x16x32_bf16 v[100:103], v[178:181], v[218:221], v[100:103]
	v_mfma_f32_16x16x32_bf16 v[92:95], v[170:173], v[226:229], v[92:95]
	v_mfma_f32_16x16x32_bf16 v[84:87], v[178:181], v[226:229], v[84:87]
	s_setprio 0
	s_setprio 1
	v_mfma_f32_16x16x32_bf16 v[104:107], v[182:185], v[198:201], v[104:107]
	v_mfma_f32_16x16x32_bf16 v[96:99], v[190:193], v[198:201], v[96:99]
	v_mfma_f32_16x16x32_bf16 v[88:91], v[182:185], v[206:209], v[88:91]
	v_mfma_f32_16x16x32_bf16 v[80:83], v[190:193], v[206:209], v[80:83]
	v_mfma_f32_16x16x32_bf16 v[76:79], v[182:185], v[214:217], v[76:79]
	v_mfma_f32_16x16x32_bf16 v[72:75], v[190:193], v[214:217], v[72:75]
	v_mfma_f32_16x16x32_bf16 v[68:71], v[182:185], v[222:225], v[68:71]
	v_mfma_f32_16x16x32_bf16 v[64:67], v[190:193], v[222:225], v[64:67]
	v_mfma_f32_16x16x32_bf16 v[104:107], v[186:189], v[202:205], v[104:107]
	v_mfma_f32_16x16x32_bf16 v[96:99], v[194:197], v[202:205], v[96:99]
	v_mfma_f32_16x16x32_bf16 v[88:91], v[186:189], v[210:213], v[88:91]
	v_mfma_f32_16x16x32_bf16 v[80:83], v[194:197], v[210:213], v[80:83]
	v_mfma_f32_16x16x32_bf16 v[76:79], v[186:189], v[218:221], v[76:79]
	v_mfma_f32_16x16x32_bf16 v[72:75], v[194:197], v[218:221], v[72:75]
	v_mfma_f32_16x16x32_bf16 v[68:71], v[186:189], v[226:229], v[68:71]
	v_mfma_f32_16x16x32_bf16 v[64:67], v[194:197], v[226:229], v[64:67]
	s_setprio 0
	s_barrier
	s_add_i32 s46, s63, s1
	v_lshl_add_u64 v[232:233], v[232:233], 0, s[24:25]
	s_mov_b32 m0, s46
	ds_read_b128 v[198:201], v164 offset:49152
	ds_read_b128 v[202:205], v164 offset:50176
	ds_read_b128 v[206:209], v164 offset:51200
	ds_read_b128 v[210:213], v164 offset:52224
	ds_read_b128 v[214:217], v164 offset:53248
	ds_read_b128 v[218:221], v164 offset:54272
	ds_read_b128 v[222:225], v164 offset:55296
	ds_read_b128 v[226:229], v164 offset:56320
	global_load_lds_dwordx4 v[232:233], off
	s_add_i32 m0, s46, 0x2000
	s_add_u32 s44, s44, 0x80080
	v_lshl_add_u64 v[232:233], v[234:235], 0, s[24:25]
	s_addc_u32 s45, s45, 0
	s_add_i32 s46, s64, s1
	global_load_lds_dwordx4 v[232:233], off
	v_lshl_add_u64 v[232:233], s[44:45], 0, v[146:147]
	s_mov_b32 m0, s46
	v_lshl_add_u64 v[230:231], v[230:231], 0, s[24:25]
	global_load_lds_dwordx4 v[232:233], off
	v_lshl_add_u64 v[232:233], s[44:45], 0, v[148:149]
	s_add_i32 m0, s46, 0x2000
	s_nop 0
	global_load_lds_dwordx4 v[232:233], off
	v_lshl_add_u64 v[232:233], v[236:237], 0, s[24:25]
	s_mov_b32 m0, s9
	s_nop 0
	global_load_lds_dwordx4 v[232:233], off
	s_mov_b32 m0, s48
	s_nop 0
	global_load_lds_dwordx4 v[230:231], off
	s_waitcnt vmcnt(8)
	s_waitcnt lgkmcnt(0)
	s_barrier
	s_setprio 1
	s_waitcnt lgkmcnt(0)
	v_mfma_f32_16x16x32_bf16 v[60:63], v[140:143], v[198:201], v[60:63]
	v_mfma_f32_16x16x32_bf16 v[56:59], v[174:177], v[198:201], v[56:59]
	v_mfma_f32_16x16x32_bf16 v[44:47], v[140:143], v[206:209], v[44:47]
	v_mfma_f32_16x16x32_bf16 v[36:39], v[174:177], v[206:209], v[36:39]
	v_mfma_f32_16x16x32_bf16 v[20:23], v[140:143], v[214:217], v[20:23]
	v_mfma_f32_16x16x32_bf16 v[12:15], v[174:177], v[214:217], v[12:15]
	v_mfma_f32_16x16x32_bf16 v[4:7], v[140:143], v[222:225], v[4:7]
	v_mfma_f32_16x16x32_bf16 v[0:3], v[174:177], v[222:225], v[0:3]
	v_mfma_f32_16x16x32_bf16 v[60:63], v[170:173], v[202:205], v[60:63]
	v_mfma_f32_16x16x32_bf16 v[56:59], v[178:181], v[202:205], v[56:59]
	v_mfma_f32_16x16x32_bf16 v[44:47], v[170:173], v[210:213], v[44:47]
	v_mfma_f32_16x16x32_bf16 v[36:39], v[178:181], v[210:213], v[36:39]
	v_mfma_f32_16x16x32_bf16 v[20:23], v[170:173], v[218:221], v[20:23]
	v_mfma_f32_16x16x32_bf16 v[12:15], v[178:181], v[218:221], v[12:15]
	v_mfma_f32_16x16x32_bf16 v[4:7], v[170:173], v[226:229], v[4:7]
	v_mfma_f32_16x16x32_bf16 v[0:3], v[178:181], v[226:229], v[0:3]
	s_setprio 0
	s_setprio 1
	v_mfma_f32_16x16x32_bf16 v[40:43], v[182:185], v[198:201], v[40:43]
	v_mfma_f32_16x16x32_bf16 v[32:35], v[190:193], v[198:201], v[32:35]
	v_mfma_f32_16x16x32_bf16 v[16:19], v[182:185], v[206:209], v[16:19]
	v_mfma_f32_16x16x32_bf16 v[8:11], v[190:193], v[206:209], v[8:11]
	v_mfma_f32_16x16x32_bf16 v[48:51], v[182:185], v[214:217], v[48:51]
	v_mfma_f32_16x16x32_bf16 v[52:55], v[190:193], v[214:217], v[52:55]
	v_mfma_f32_16x16x32_bf16 v[24:27], v[182:185], v[222:225], v[24:27]
	v_mfma_f32_16x16x32_bf16 v[28:31], v[190:193], v[222:225], v[28:31]
	v_mfma_f32_16x16x32_bf16 v[40:43], v[186:189], v[202:205], v[40:43]
	v_mfma_f32_16x16x32_bf16 v[32:35], v[194:197], v[202:205], v[32:35]
	v_mfma_f32_16x16x32_bf16 v[16:19], v[186:189], v[210:213], v[16:19]
	v_mfma_f32_16x16x32_bf16 v[8:11], v[194:197], v[210:213], v[8:11]
	v_mfma_f32_16x16x32_bf16 v[48:51], v[186:189], v[218:221], v[48:51]
	v_mfma_f32_16x16x32_bf16 v[52:55], v[194:197], v[218:221], v[52:55]
	v_mfma_f32_16x16x32_bf16 v[24:27], v[186:189], v[226:229], v[24:27]
	v_mfma_f32_16x16x32_bf16 v[28:31], v[194:197], v[226:229], v[28:31]
	s_setprio 0
	s_add_i32 s62, s62, 2
	s_add_u32 s12, s12, 0x100
	s_addc_u32 s13, s13, 0
	s_cmp_gt_u32 s62, 29
	s_barrier
	s_cbranch_scc0 .LBB0_964
	s_and_b64 vcc, exec, s[26:27]
	s_cbranch_vccz .LBB0_967
	s_barrier

.LBB0_1359:
	v_add_u32_e32 v165, s51, v143
	ds_read_b128 v[166:169], v165
	ds_read_b128 v[170:173], v165 offset:1024
	ds_read_b128 v[174:177], v165 offset:2048
	ds_read_b128 v[178:181], v165 offset:3072
	v_add_u32_e32 v165, s52, v143
	ds_read_b128 v[182:185], v165
	ds_read_b128 v[186:189], v165 offset:1024
	ds_read_b128 v[190:193], v165 offset:2048
	ds_read_b128 v[194:197], v165 offset:3072
	s_cmpk_eq_i32 s14, 0x1000
	s_cselect_b64 vcc, -1, 0
	s_and_b64 s[48:49], vcc, exec
	s_cselect_b32 s48, 0, s14
	v_lshl_add_u64 v[154:155], v[148:149], 0, s[14:15]
	s_cselect_b32 s49, 0, s15
	s_add_u32 s48, s22, s48
	v_cndmask_b32_e32 v132, v146, v160, vcc
	v_cndmask_b32_e32 v139, v140, v162, vcc
	v_cndmask_b32_e32 v230, v142, v161, vcc
	v_cndmask_b32_e32 v141, v138, v163, vcc
	v_cndmask_b32_e32 v154, v154, v164, vcc
	v_cndmask_b32_e32 v155, v155, v135, vcc
	s_addc_u32 s49, s23, s49
	v_lshl_add_u64 v[232:233], v[152:153], 0, s[14:15]
	s_mov_b32 m0, s53
	v_lshl_add_u64 v[232:233], v[232:233], 0, s[42:43]
	ds_read_b128 v[198:201], v159
	ds_read_b128 v[202:205], v159 offset:1024
	ds_read_b128 v[206:209], v159 offset:2048
	ds_read_b128 v[210:213], v159 offset:3072
	ds_read_b128 v[214:217], v159 offset:4096
	ds_read_b128 v[218:221], v159 offset:5120
	ds_read_b128 v[222:225], v159 offset:6144
	ds_read_b128 v[226:229], v159 offset:7168
	global_load_lds_dwordx4 v[232:233], off
	v_lshl_add_u64 v[232:233], v[150:151], 0, s[14:15]
	v_lshl_add_u64 v[232:233], v[232:233], 0, s[42:43]
	s_mov_b32 m0, s55
	s_nop 0
	global_load_lds_dwordx4 v[232:233], off
	s_waitcnt vmcnt(8)
	s_waitcnt lgkmcnt(0)
	s_barrier
	s_setprio 1
	s_waitcnt lgkmcnt(0)
	v_mfma_f32_16x16x32_bf16 v[124:127], v[166:169], v[198:201], v[124:127]
	v_mfma_f32_16x16x32_bf16 v[120:123], v[174:177], v[198:201], v[120:123]
	v_mfma_f32_16x16x32_bf16 v[108:111], v[166:169], v[206:209], v[108:111]
	v_mfma_f32_16x16x32_bf16 v[104:107], v[174:177], v[206:209], v[104:107]
	v_mfma_f32_16x16x32_bf16 v[92:95], v[166:169], v[214:217], v[92:95]
	v_mfma_f32_16x16x32_bf16 v[88:91], v[174:177], v[214:217], v[88:91]
	v_mfma_f32_16x16x32_bf16 v[76:79], v[166:169], v[222:225], v[76:79]
	v_mfma_f32_16x16x32_bf16 v[72:75], v[174:177], v[222:225], v[72:75]
	v_mfma_f32_16x16x32_bf16 v[124:127], v[170:173], v[202:205], v[124:127]
	v_mfma_f32_16x16x32_bf16 v[120:123], v[178:181], v[202:205], v[120:123]
	v_mfma_f32_16x16x32_bf16 v[108:111], v[170:173], v[210:213], v[108:111]
	v_mfma_f32_16x16x32_bf16 v[104:107], v[178:181], v[210:213], v[104:107]
	v_mfma_f32_16x16x32_bf16 v[92:95], v[170:173], v[218:221], v[92:95]
	v_mfma_f32_16x16x32_bf16 v[88:91], v[178:181], v[218:221], v[88:91]
	v_mfma_f32_16x16x32_bf16 v[76:79], v[170:173], v[226:229], v[76:79]
	v_mfma_f32_16x16x32_bf16 v[72:75], v[178:181], v[226:229], v[72:75]
	s_setprio 0
	s_setprio 1
	v_mfma_f32_16x16x32_bf16 v[116:119], v[182:185], v[198:201], v[116:119]
	v_mfma_f32_16x16x32_bf16 v[112:115], v[190:193], v[198:201], v[112:115]
	v_mfma_f32_16x16x32_bf16 v[100:103], v[182:185], v[206:209], v[100:103]
	v_mfma_f32_16x16x32_bf16 v[96:99], v[190:193], v[206:209], v[96:99]
	v_mfma_f32_16x16x32_bf16 v[84:87], v[182:185], v[214:217], v[84:87]
	v_mfma_f32_16x16x32_bf16 v[80:83], v[190:193], v[214:217], v[80:83]
	v_mfma_f32_16x16x32_bf16 v[68:71], v[182:185], v[222:225], v[68:71]
	v_mfma_f32_16x16x32_bf16 v[64:67], v[190:193], v[222:225], v[64:67]
	v_mfma_f32_16x16x32_bf16 v[116:119], v[186:189], v[202:205], v[116:119]
	v_mfma_f32_16x16x32_bf16 v[112:115], v[194:197], v[202:205], v[112:115]
	v_mfma_f32_16x16x32_bf16 v[100:103], v[186:189], v[210:213], v[100:103]
	v_mfma_f32_16x16x32_bf16 v[96:99], v[194:197], v[210:213], v[96:99]
	v_mfma_f32_16x16x32_bf16 v[84:87], v[186:189], v[218:221], v[84:87]
	v_mfma_f32_16x16x32_bf16 v[80:83], v[194:197], v[218:221], v[80:83]
	v_mfma_f32_16x16x32_bf16 v[68:71], v[186:189], v[226:229], v[68:71]
	v_mfma_f32_16x16x32_bf16 v[64:67], v[194:197], v[226:229], v[64:67]
	s_setprio 0
	s_barrier
	s_mov_b32 m0, s57
	v_lshl_add_u64 v[232:233], v[154:155], 0, v[128:129]
	ds_read_b128 v[198:201], v159 offset:16384
	ds_read_b128 v[202:205], v159 offset:17408
	ds_read_b128 v[206:209], v159 offset:18432
	ds_read_b128 v[210:213], v159 offset:19456
	ds_read_b128 v[214:217], v159 offset:20480
	ds_read_b128 v[218:221], v159 offset:21504
	ds_read_b128 v[222:225], v159 offset:22528
	ds_read_b128 v[226:229], v159 offset:23552
	global_load_lds_dwordx4 v[232:233], off
	v_lshl_add_u64 v[234:235], v[154:155], 0, v[130:131]
	s_mov_b32 m0, s59
	v_lshl_add_u64 v[236:237], v[154:155], 0, s[30:31]
	global_load_lds_dwordx4 v[234:235], off
	v_lshl_add_u64 v[238:239], v[236:237], 0, v[128:129]
	s_mov_b32 m0, s60
	v_lshl_add_u64 v[236:237], v[236:237], 0, v[130:131]
	global_load_lds_dwordx4 v[238:239], off
	s_mov_b32 m0, s61
	v_mov_b32_e32 v231, v133
	global_load_lds_dwordx4 v[236:237], off
	s_mov_b32 m0, s1
	v_lshl_add_u64 v[236:237], s[48:49], 0, v[132:133]
	global_load_lds_dwordx4 v132, s[48:49]
	s_mov_b32 m0, s4
	s_nop 0
	global_load_lds_dwordx4 v230, s[48:49]
	s_waitcnt vmcnt(8)
	s_waitcnt lgkmcnt(0)
	v_lshl_add_u64 v[230:231], s[48:49], 0, v[230:231]
	s_barrier
	s_setprio 1
	s_waitcnt lgkmcnt(0)
	v_mfma_f32_16x16x32_bf16 v[60:63], v[166:169], v[198:201], v[60:63]
	v_mfma_f32_16x16x32_bf16 v[56:59], v[174:177], v[198:201], v[56:59]
	v_mfma_f32_16x16x32_bf16 v[44:47], v[166:169], v[206:209], v[44:47]
	v_mfma_f32_16x16x32_bf16 v[36:39], v[174:177], v[206:209], v[36:39]
	v_mfma_f32_16x16x32_bf16 v[20:23], v[166:169], v[214:217], v[20:23]
	v_mfma_f32_16x16x32_bf16 v[8:11], v[174:177], v[214:217], v[8:11]
	v_mfma_f32_16x16x32_bf16 v[4:7], v[166:169], v[222:225], v[4:7]
	v_mfma_f32_16x16x32_bf16 v[0:3], v[174:177], v[222:225], v[0:3]
	v_mfma_f32_16x16x32_bf16 v[60:63], v[170:173], v[202:205], v[60:63]
	v_mfma_f32_16x16x32_bf16 v[56:59], v[178:181], v[202:205], v[56:59]
	v_mfma_f32_16x16x32_bf16 v[44:47], v[170:173], v[210:213], v[44:47]
	v_mfma_f32_16x16x32_bf16 v[36:39], v[178:181], v[210:213], v[36:39]
	v_mfma_f32_16x16x32_bf16 v[20:23], v[170:173], v[218:221], v[20:23]
	v_mfma_f32_16x16x32_bf16 v[8:11], v[178:181], v[218:221], v[8:11]
	v_mfma_f32_16x16x32_bf16 v[4:7], v[170:173], v[226:229], v[4:7]
	v_mfma_f32_16x16x32_bf16 v[0:3], v[178:181], v[226:229], v[0:3]
	s_setprio 0
	s_setprio 1
	v_mfma_f32_16x16x32_bf16 v[52:55], v[182:185], v[198:201], v[52:55]
	v_mfma_f32_16x16x32_bf16 v[48:51], v[190:193], v[198:201], v[48:51]
	v_mfma_f32_16x16x32_bf16 v[28:31], v[182:185], v[206:209], v[28:31]
	v_mfma_f32_16x16x32_bf16 v[24:27], v[190:193], v[206:209], v[24:27]
	v_mfma_f32_16x16x32_bf16 v[40:43], v[182:185], v[214:217], v[40:43]
	v_mfma_f32_16x16x32_bf16 v[32:35], v[190:193], v[214:217], v[32:35]
	v_mfma_f32_16x16x32_bf16 v[16:19], v[182:185], v[222:225], v[16:19]
	v_mfma_f32_16x16x32_bf16 v[12:15], v[190:193], v[222:225], v[12:15]
	v_mfma_f32_16x16x32_bf16 v[52:55], v[186:189], v[202:205], v[52:55]
	v_mfma_f32_16x16x32_bf16 v[48:51], v[194:197], v[202:205], v[48:51]
	v_mfma_f32_16x16x32_bf16 v[28:31], v[186:189], v[210:213], v[28:31]
	v_mfma_f32_16x16x32_bf16 v[24:27], v[194:197], v[210:213], v[24:27]
	v_mfma_f32_16x16x32_bf16 v[40:43], v[186:189], v[218:221], v[40:43]
	v_mfma_f32_16x16x32_bf16 v[32:35], v[194:197], v[218:221], v[32:35]
	v_mfma_f32_16x16x32_bf16 v[16:19], v[186:189], v[226:229], v[16:19]
	v_mfma_f32_16x16x32_bf16 v[12:15], v[194:197], v[226:229], v[12:15]
	s_setprio 0
	s_barrier
	v_add_u32_e32 v132, s62, v143
	ds_read_b128 v[166:169], v132
	ds_read_b128 v[170:173], v132 offset:1024
	ds_read_b128 v[174:177], v132 offset:2048
	ds_read_b128 v[178:181], v132 offset:3072
	v_add_u32_e32 v132, s63, v143
	ds_read_b128 v[182:185], v132
	ds_read_b128 v[186:189], v132 offset:1024
	ds_read_b128 v[190:193], v132 offset:2048
	ds_read_b128 v[194:197], v132 offset:3072
	s_mov_b32 m0, s5
	ds_read_b128 v[198:201], v159 offset:32768
	ds_read_b128 v[202:205], v159 offset:33792
	ds_read_b128 v[206:209], v159 offset:34816
	ds_read_b128 v[210:213], v159 offset:35840
	ds_read_b128 v[214:217], v159 offset:36864
	ds_read_b128 v[218:221], v159 offset:37888
	ds_read_b128 v[222:225], v159 offset:38912
	ds_read_b128 v[226:229], v159 offset:39936
	global_load_lds_dwordx4 v139, s[48:49]
	s_mov_b32 m0, s6
	s_nop 0
	global_load_lds_dwordx4 v141, s[48:49]
	s_waitcnt vmcnt(8)
	s_waitcnt lgkmcnt(0)
	s_barrier
	s_setprio 1
	s_waitcnt lgkmcnt(0)
	v_mfma_f32_16x16x32_bf16 v[124:127], v[166:169], v[198:201], v[124:127]
	v_mfma_f32_16x16x32_bf16 v[120:123], v[174:177], v[198:201], v[120:123]
	v_mfma_f32_16x16x32_bf16 v[108:111], v[166:169], v[206:209], v[108:111]
	v_mfma_f32_16x16x32_bf16 v[104:107], v[174:177], v[206:209], v[104:107]
	v_mfma_f32_16x16x32_bf16 v[92:95], v[166:169], v[214:217], v[92:95]
	v_mfma_f32_16x16x32_bf16 v[88:91], v[174:177], v[214:217], v[88:91]
	v_mfma_f32_16x16x32_bf16 v[76:79], v[166:169], v[222:225], v[76:79]
	v_mfma_f32_16x16x32_bf16 v[72:75], v[174:177], v[222:225], v[72:75]
	v_mfma_f32_16x16x32_bf16 v[124:127], v[170:173], v[202:205], v[124:127]
	v_mfma_f32_16x16x32_bf16 v[120:123], v[178:181], v[202:205], v[120:123]
	v_mfma_f32_16x16x32_bf16 v[108:111], v[170:173], v[210:213], v[108:111]
	v_mfma_f32_16x16x32_bf16 v[104:107], v[178:181], v[210:213], v[104:107]
	v_mfma_f32_16x16x32_bf16 v[92:95], v[170:173], v[218:221], v[92:95]
	v_mfma_f32_16x16x32_bf16 v[88:91], v[178:181], v[218:221], v[88:91]
	v_mfma_f32_16x16x32_bf16 v[76:79], v[170:173], v[226:229], v[76:79]
	v_mfma_f32_16x16x32_bf16 v[72:75], v[178:181], v[226:229], v[72:75]
	s_setprio 0
	s_setprio 1
	v_mfma_f32_16x16x32_bf16 v[116:119], v[182:185], v[198:201], v[116:119]
	v_mfma_f32_16x16x32_bf16 v[112:115], v[190:193], v[198:201], v[112:115]
	v_mfma_f32_16x16x32_bf16 v[100:103], v[182:185], v[206:209], v[100:103]
	v_mfma_f32_16x16x32_bf16 v[96:99], v[190:193], v[206:209], v[96:99]
	v_mfma_f32_16x16x32_bf16 v[84:87], v[182:185], v[214:217], v[84:87]
	v_mfma_f32_16x16x32_bf16 v[80:83], v[190:193], v[214:217], v[80:83]
	v_mfma_f32_16x16x32_bf16 v[68:71], v[182:185], v[222:225], v[68:71]
	v_mfma_f32_16x16x32_bf16 v[64:67], v[190:193], v[222:225], v[64:67]
	v_mfma_f32_16x16x32_bf16 v[116:119], v[186:189], v[202:205], v[116:119]
	v_mfma_f32_16x16x32_bf16 v[112:115], v[194:197], v[202:205], v[112:115]
	v_mfma_f32_16x16x32_bf16 v[100:103], v[186:189], v[210:213], v[100:103]
	v_mfma_f32_16x16x32_bf16 v[96:99], v[194:197], v[210:213], v[96:99]
	v_mfma_f32_16x16x32_bf16 v[84:87], v[186:189], v[218:221], v[84:87]
	v_mfma_f32_16x16x32_bf16 v[80:83], v[194:197], v[218:221], v[80:83]
	v_mfma_f32_16x16x32_bf16 v[68:71], v[186:189], v[226:229], v[68:71]
	v_mfma_f32_16x16x32_bf16 v[64:67], v[194:197], v[226:229], v[64:67]
	s_setprio 0
	s_barrier
	s_add_i32 s48, s62, s0
	v_lshl_add_u64 v[232:233], v[232:233], 0, s[36:37]
	s_mov_b32 m0, s48
	ds_read_b128 v[198:201], v159 offset:49152
	ds_read_b128 v[202:205], v159 offset:50176
	ds_read_b128 v[206:209], v159 offset:51200
	ds_read_b128 v[210:213], v159 offset:52224
	ds_read_b128 v[214:217], v159 offset:53248
	ds_read_b128 v[218:221], v159 offset:54272
	ds_read_b128 v[222:225], v159 offset:55296
	ds_read_b128 v[226:229], v159 offset:56320
	global_load_lds_dwordx4 v[232:233], off
	v_lshl_add_u64 v[232:233], v[234:235], 0, s[36:37]
	s_add_i32 m0, s48, 0x2000
	v_lshl_add_u64 v[154:155], v[154:155], 0, s[38:39]
	s_add_i32 s48, s63, s0
	global_load_lds_dwordx4 v[232:233], off
	v_lshl_add_u64 v[232:233], v[154:155], 0, v[128:129]
	s_mov_b32 m0, s48
	v_lshl_add_u64 v[154:155], v[154:155], 0, v[130:131]
	global_load_lds_dwordx4 v[232:233], off
	s_add_i32 m0, s48, 0x2000
	s_nop 0
	global_load_lds_dwordx4 v[154:155], off
	v_lshl_add_u64 v[154:155], v[236:237], 0, s[36:37]
	s_mov_b32 m0, s9
	s_nop 0
	global_load_lds_dwordx4 v[154:155], off
	v_lshl_add_u64 v[154:155], v[230:231], 0, s[36:37]
	s_mov_b32 m0, s28
	s_nop 0
	global_load_lds_dwordx4 v[154:155], off
	s_waitcnt vmcnt(8)
	s_waitcnt lgkmcnt(0)
	s_barrier
	s_setprio 1
	s_waitcnt lgkmcnt(0)
	v_mfma_f32_16x16x32_bf16 v[60:63], v[166:169], v[198:201], v[60:63]
	v_mfma_f32_16x16x32_bf16 v[56:59], v[174:177], v[198:201], v[56:59]
	v_mfma_f32_16x16x32_bf16 v[44:47], v[166:169], v[206:209], v[44:47]
	v_mfma_f32_16x16x32_bf16 v[36:39], v[174:177], v[206:209], v[36:39]
	v_mfma_f32_16x16x32_bf16 v[20:23], v[166:169], v[214:217], v[20:23]
	v_mfma_f32_16x16x32_bf16 v[8:11], v[174:177], v[214:217], v[8:11]
	v_mfma_f32_16x16x32_bf16 v[4:7], v[166:169], v[222:225], v[4:7]
	v_mfma_f32_16x16x32_bf16 v[0:3], v[174:177], v[222:225], v[0:3]
	v_mfma_f32_16x16x32_bf16 v[60:63], v[170:173], v[202:205], v[60:63]
	v_mfma_f32_16x16x32_bf16 v[56:59], v[178:181], v[202:205], v[56:59]
	v_mfma_f32_16x16x32_bf16 v[44:47], v[170:173], v[210:213], v[44:47]
	v_mfma_f32_16x16x32_bf16 v[36:39], v[178:181], v[210:213], v[36:39]
	v_mfma_f32_16x16x32_bf16 v[20:23], v[170:173], v[218:221], v[20:23]
	v_mfma_f32_16x16x32_bf16 v[8:11], v[178:181], v[218:221], v[8:11]
	v_mfma_f32_16x16x32_bf16 v[4:7], v[170:173], v[226:229], v[4:7]
	v_mfma_f32_16x16x32_bf16 v[0:3], v[178:181], v[226:229], v[0:3]
	s_setprio 0
	s_setprio 1
	v_mfma_f32_16x16x32_bf16 v[52:55], v[182:185], v[198:201], v[52:55]
	v_mfma_f32_16x16x32_bf16 v[48:51], v[190:193], v[198:201], v[48:51]
	v_mfma_f32_16x16x32_bf16 v[28:31], v[182:185], v[206:209], v[28:31]
	v_mfma_f32_16x16x32_bf16 v[24:27], v[190:193], v[206:209], v[24:27]
	v_mfma_f32_16x16x32_bf16 v[40:43], v[182:185], v[214:217], v[40:43]
	v_mfma_f32_16x16x32_bf16 v[32:35], v[190:193], v[214:217], v[32:35]
	v_mfma_f32_16x16x32_bf16 v[16:19], v[182:185], v[222:225], v[16:19]
	v_mfma_f32_16x16x32_bf16 v[12:15], v[190:193], v[222:225], v[12:15]
	v_mfma_f32_16x16x32_bf16 v[52:55], v[186:189], v[202:205], v[52:55]
	v_mfma_f32_16x16x32_bf16 v[48:51], v[194:197], v[202:205], v[48:51]
	v_mfma_f32_16x16x32_bf16 v[28:31], v[186:189], v[210:213], v[28:31]
	v_mfma_f32_16x16x32_bf16 v[24:27], v[194:197], v[210:213], v[24:27]
	v_mfma_f32_16x16x32_bf16 v[40:43], v[186:189], v[218:221], v[40:43]
	v_mfma_f32_16x16x32_bf16 v[32:35], v[194:197], v[218:221], v[32:35]
	v_mfma_f32_16x16x32_bf16 v[16:19], v[186:189], v[226:229], v[16:19]
	v_mfma_f32_16x16x32_bf16 v[12:15], v[194:197], v[226:229], v[12:15]
	s_setprio 0
	s_add_i32 s47, s47, 2
	s_add_u32 s14, s14, 0x100
	s_addc_u32 s15, s15, 0
	s_cmp_gt_u32 s47, 29
	s_barrier
	s_cbranch_scc0 .LBB0_1359
	s_and_b64 vcc, exec, s[40:41]
	s_cbranch_vccz .LBB0_1362
	s_barrier

.LBB0_1571:
	ds_read_b128 v[170:173], v163
	ds_read_b128 v[174:177], v163 offset:1024
	ds_read_b128 v[178:181], v163 offset:2048
	ds_read_b128 v[182:185], v163 offset:3072
	ds_read_b128 v[186:189], v164
	ds_read_b128 v[190:193], v164 offset:1024
	ds_read_b128 v[194:197], v164 offset:2048
	ds_read_b128 v[198:201], v164 offset:3072
	s_add_u32 s46, s42, s10
	s_addc_u32 s47, s43, s11
	s_cmpk_eq_i32 s10, 0x1000
	s_cselect_b64 vcc, -1, 0
	s_and_b64 s[44:45], vcc, exec
	s_cselect_b32 s64, 0, s10
	s_cselect_b32 s63, 0, s11
	s_cselect_b32 s44, s39, s46
	s_cselect_b32 s45, s13, s47
	s_add_u32 s46, s20, s64
	v_cndmask_b32_e32 v140, v128, v166, vcc
	v_cndmask_b32_e32 v129, v132, v168, vcc
	v_cndmask_b32_e32 v154, v130, v167, vcc
	v_cndmask_b32_e32 v131, v134, v169, vcc
	s_addc_u32 s47, s21, s63
	v_lshl_add_u64 v[234:235], v[152:153], 0, s[10:11]
	v_lshl_add_u64 v[234:235], v[234:235], 0, s[18:19]
	s_add_i32 m0, s5, 0xc000
	ds_read_b128 v[202:205], v165
	ds_read_b128 v[206:209], v165 offset:1024
	ds_read_b128 v[210:213], v165 offset:2048
	ds_read_b128 v[214:217], v165 offset:3072
	ds_read_b128 v[218:221], v165 offset:4096
	ds_read_b128 v[222:225], v165 offset:5120
	ds_read_b128 v[226:229], v165 offset:6144
	ds_read_b128 v[230:233], v165 offset:7168
	global_load_lds_dwordx4 v[234:235], off
	v_lshl_add_u64 v[234:235], v[150:151], 0, s[10:11]
	v_lshl_add_u64 v[234:235], v[234:235], 0, s[18:19]
	s_add_i32 m0, s5, 0xe000
	s_nop 0
	global_load_lds_dwordx4 v[234:235], off
	s_waitcnt vmcnt(8)
	s_waitcnt lgkmcnt(0)
	s_barrier
	s_setprio 1
	s_waitcnt lgkmcnt(0)
	v_mfma_f32_16x16x32_bf16 v[60:63], v[170:173], v[202:205], v[60:63]
	v_mfma_f32_16x16x32_bf16 v[56:59], v[178:181], v[202:205], v[56:59]
	v_mfma_f32_16x16x32_bf16 v[52:55], v[170:173], v[210:213], v[52:55]
	v_mfma_f32_16x16x32_bf16 v[48:51], v[178:181], v[210:213], v[48:51]
	v_mfma_f32_16x16x32_bf16 v[44:47], v[170:173], v[218:221], v[44:47]
	v_mfma_f32_16x16x32_bf16 v[40:43], v[178:181], v[218:221], v[40:43]
	v_mfma_f32_16x16x32_bf16 v[36:39], v[170:173], v[226:229], v[36:39]
	v_mfma_f32_16x16x32_bf16 v[32:35], v[178:181], v[226:229], v[32:35]
	v_mfma_f32_16x16x32_bf16 v[60:63], v[174:177], v[206:209], v[60:63]
	v_mfma_f32_16x16x32_bf16 v[56:59], v[182:185], v[206:209], v[56:59]
	v_mfma_f32_16x16x32_bf16 v[52:55], v[174:177], v[214:217], v[52:55]
	v_mfma_f32_16x16x32_bf16 v[48:51], v[182:185], v[214:217], v[48:51]
	v_mfma_f32_16x16x32_bf16 v[44:47], v[174:177], v[222:225], v[44:47]
	v_mfma_f32_16x16x32_bf16 v[40:43], v[182:185], v[222:225], v[40:43]
	v_mfma_f32_16x16x32_bf16 v[36:39], v[174:177], v[230:233], v[36:39]
	v_mfma_f32_16x16x32_bf16 v[32:35], v[182:185], v[230:233], v[32:35]
	s_setprio 0
	s_setprio 1
	v_mfma_f32_16x16x32_bf16 v[124:127], v[186:189], v[202:205], v[124:127]
	v_mfma_f32_16x16x32_bf16 v[120:123], v[194:197], v[202:205], v[120:123]
	v_mfma_f32_16x16x32_bf16 v[116:119], v[186:189], v[210:213], v[116:119]
	v_mfma_f32_16x16x32_bf16 v[112:115], v[194:197], v[210:213], v[112:115]
	v_mfma_f32_16x16x32_bf16 v[108:111], v[186:189], v[218:221], v[108:111]
	v_mfma_f32_16x16x32_bf16 v[104:107], v[194:197], v[218:221], v[104:107]
	v_mfma_f32_16x16x32_bf16 v[100:103], v[186:189], v[226:229], v[100:103]
	v_mfma_f32_16x16x32_bf16 v[96:99], v[194:197], v[226:229], v[96:99]
	v_mfma_f32_16x16x32_bf16 v[124:127], v[190:193], v[206:209], v[124:127]
	v_mfma_f32_16x16x32_bf16 v[120:123], v[198:201], v[206:209], v[120:123]
	v_mfma_f32_16x16x32_bf16 v[116:119], v[190:193], v[214:217], v[116:119]
	v_mfma_f32_16x16x32_bf16 v[112:115], v[198:201], v[214:217], v[112:115]
	v_mfma_f32_16x16x32_bf16 v[108:111], v[190:193], v[222:225], v[108:111]
	v_mfma_f32_16x16x32_bf16 v[104:107], v[198:201], v[222:225], v[104:107]
	v_mfma_f32_16x16x32_bf16 v[100:103], v[190:193], v[230:233], v[100:103]
	v_mfma_f32_16x16x32_bf16 v[96:99], v[198:201], v[230:233], v[96:99]
	s_setprio 0
	s_barrier
	s_add_i32 s63, s55, s0
	v_lshl_add_u64 v[234:235], s[44:45], 0, v[136:137]
	s_mov_b32 m0, s63
	ds_read_b128 v[202:205], v165 offset:16384
	ds_read_b128 v[206:209], v165 offset:17408
	ds_read_b128 v[210:213], v165 offset:18432
	ds_read_b128 v[214:217], v165 offset:19456
	ds_read_b128 v[218:221], v165 offset:20480
	ds_read_b128 v[222:225], v165 offset:21504
	ds_read_b128 v[226:229], v165 offset:22528
	ds_read_b128 v[230:233], v165 offset:23552
	global_load_lds_dwordx4 v[234:235], off
	s_add_i32 m0, s63, 0x2000
	s_add_u32 s64, s44, 0x80000
	v_lshl_add_u64 v[236:237], s[44:45], 0, v[138:139]
	s_addc_u32 s65, s45, 0
	s_add_i32 s63, s57, s0
	global_load_lds_dwordx4 v[236:237], off
	v_lshl_add_u64 v[238:239], s[64:65], 0, v[136:137]
	s_mov_b32 m0, s63
	v_mov_b32_e32 v155, v141
	global_load_lds_dwordx4 v[238:239], off
	v_lshl_add_u64 v[238:239], s[64:65], 0, v[138:139]
	s_add_i32 m0, s63, 0x2000
	s_nop 0
	global_load_lds_dwordx4 v[238:239], off
	s_mov_b32 m0, s5
	v_lshl_add_u64 v[238:239], s[46:47], 0, v[140:141]
	global_load_lds_dwordx4 v140, s[46:47]
	s_mov_b32 m0, s6
	s_nop 0
	global_load_lds_dwordx4 v154, s[46:47]
	s_waitcnt vmcnt(8)
	s_waitcnt lgkmcnt(0)
	v_lshl_add_u64 v[154:155], s[46:47], 0, v[154:155]
	s_barrier
	s_setprio 1
	s_waitcnt lgkmcnt(0)
	v_mfma_f32_16x16x32_bf16 v[28:31], v[170:173], v[202:205], v[28:31]
	v_mfma_f32_16x16x32_bf16 v[24:27], v[178:181], v[202:205], v[24:27]
	v_mfma_f32_16x16x32_bf16 v[20:23], v[170:173], v[210:213], v[20:23]
	v_mfma_f32_16x16x32_bf16 v[16:19], v[178:181], v[210:213], v[16:19]
	v_mfma_f32_16x16x32_bf16 v[12:15], v[170:173], v[218:221], v[12:15]
	v_mfma_f32_16x16x32_bf16 v[8:11], v[178:181], v[218:221], v[8:11]
	v_mfma_f32_16x16x32_bf16 v[4:7], v[170:173], v[226:229], v[4:7]
	v_mfma_f32_16x16x32_bf16 v[0:3], v[178:181], v[226:229], v[0:3]
	v_mfma_f32_16x16x32_bf16 v[28:31], v[174:177], v[206:209], v[28:31]
	v_mfma_f32_16x16x32_bf16 v[24:27], v[182:185], v[206:209], v[24:27]
	v_mfma_f32_16x16x32_bf16 v[20:23], v[174:177], v[214:217], v[20:23]
	v_mfma_f32_16x16x32_bf16 v[16:19], v[182:185], v[214:217], v[16:19]
	v_mfma_f32_16x16x32_bf16 v[12:15], v[174:177], v[222:225], v[12:15]
	v_mfma_f32_16x16x32_bf16 v[8:11], v[182:185], v[222:225], v[8:11]
	v_mfma_f32_16x16x32_bf16 v[4:7], v[174:177], v[230:233], v[4:7]
	v_mfma_f32_16x16x32_bf16 v[0:3], v[182:185], v[230:233], v[0:3]
	s_setprio 0
	s_setprio 1
	v_mfma_f32_16x16x32_bf16 v[92:95], v[186:189], v[202:205], v[92:95]
	v_mfma_f32_16x16x32_bf16 v[88:91], v[194:197], v[202:205], v[88:91]
	v_mfma_f32_16x16x32_bf16 v[84:87], v[186:189], v[210:213], v[84:87]
	v_mfma_f32_16x16x32_bf16 v[80:83], v[194:197], v[210:213], v[80:83]
	v_mfma_f32_16x16x32_bf16 v[72:75], v[186:189], v[218:221], v[72:75]
	v_mfma_f32_16x16x32_bf16 v[76:79], v[194:197], v[218:221], v[76:79]
	v_mfma_f32_16x16x32_bf16 v[64:67], v[186:189], v[226:229], v[64:67]
	v_mfma_f32_16x16x32_bf16 v[68:71], v[194:197], v[226:229], v[68:71]
	v_mfma_f32_16x16x32_bf16 v[92:95], v[190:193], v[206:209], v[92:95]
	v_mfma_f32_16x16x32_bf16 v[88:91], v[198:201], v[206:209], v[88:91]
	v_mfma_f32_16x16x32_bf16 v[84:87], v[190:193], v[214:217], v[84:87]
	v_mfma_f32_16x16x32_bf16 v[80:83], v[198:201], v[214:217], v[80:83]
	v_mfma_f32_16x16x32_bf16 v[72:75], v[190:193], v[222:225], v[72:75]
	v_mfma_f32_16x16x32_bf16 v[76:79], v[198:201], v[222:225], v[76:79]
	v_mfma_f32_16x16x32_bf16 v[64:67], v[190:193], v[230:233], v[64:67]
	v_mfma_f32_16x16x32_bf16 v[68:71], v[198:201], v[230:233], v[68:71]
	s_setprio 0
	s_barrier
	s_add_i32 s63, 0, 0x18000
	v_add_u32_e32 v133, s63, v161
	s_add_i32 s64, 0, 0x1c000
	ds_read_b128 v[170:173], v133
	ds_read_b128 v[174:177], v133 offset:1024
	ds_read_b128 v[178:181], v133 offset:2048
	ds_read_b128 v[182:185], v133 offset:3072
	v_add_u32_e32 v133, s64, v161
	ds_read_b128 v[186:189], v133
	ds_read_b128 v[190:193], v133 offset:1024
	ds_read_b128 v[194:197], v133 offset:2048
	ds_read_b128 v[198:201], v133 offset:3072
	s_mov_b32 m0, s7
	ds_read_b128 v[202:205], v165 offset:32768
	ds_read_b128 v[206:209], v165 offset:33792
	ds_read_b128 v[210:213], v165 offset:34816
	ds_read_b128 v[214:217], v165 offset:35840
	ds_read_b128 v[218:221], v165 offset:36864
	ds_read_b128 v[222:225], v165 offset:37888
	ds_read_b128 v[226:229], v165 offset:38912
	ds_read_b128 v[230:233], v165 offset:39936
	global_load_lds_dwordx4 v129, s[46:47]
	s_mov_b32 m0, s31
	s_nop 0
	global_load_lds_dwordx4 v131, s[46:47]
	s_waitcnt vmcnt(8)
	s_waitcnt lgkmcnt(0)
	s_barrier
	s_setprio 1
	s_waitcnt lgkmcnt(0)
	v_mfma_f32_16x16x32_bf16 v[60:63], v[170:173], v[202:205], v[60:63]
	v_mfma_f32_16x16x32_bf16 v[56:59], v[178:181], v[202:205], v[56:59]
	v_mfma_f32_16x16x32_bf16 v[52:55], v[170:173], v[210:213], v[52:55]
	v_mfma_f32_16x16x32_bf16 v[48:51], v[178:181], v[210:213], v[48:51]
	v_mfma_f32_16x16x32_bf16 v[44:47], v[170:173], v[218:221], v[44:47]
	v_mfma_f32_16x16x32_bf16 v[40:43], v[178:181], v[218:221], v[40:43]
	v_mfma_f32_16x16x32_bf16 v[36:39], v[170:173], v[226:229], v[36:39]
	v_mfma_f32_16x16x32_bf16 v[32:35], v[178:181], v[226:229], v[32:35]
	v_mfma_f32_16x16x32_bf16 v[60:63], v[174:177], v[206:209], v[60:63]
	v_mfma_f32_16x16x32_bf16 v[56:59], v[182:185], v[206:209], v[56:59]
	v_mfma_f32_16x16x32_bf16 v[52:55], v[174:177], v[214:217], v[52:55]
	v_mfma_f32_16x16x32_bf16 v[48:51], v[182:185], v[214:217], v[48:51]
	v_mfma_f32_16x16x32_bf16 v[44:47], v[174:177], v[222:225], v[44:47]
	v_mfma_f32_16x16x32_bf16 v[40:43], v[182:185], v[222:225], v[40:43]
	v_mfma_f32_16x16x32_bf16 v[36:39], v[174:177], v[230:233], v[36:39]
	v_mfma_f32_16x16x32_bf16 v[32:35], v[182:185], v[230:233], v[32:35]
	s_setprio 0
	s_setprio 1
	v_mfma_f32_16x16x32_bf16 v[124:127], v[186:189], v[202:205], v[124:127]
	v_mfma_f32_16x16x32_bf16 v[120:123], v[194:197], v[202:205], v[120:123]
	v_mfma_f32_16x16x32_bf16 v[116:119], v[186:189], v[210:213], v[116:119]
	v_mfma_f32_16x16x32_bf16 v[112:115], v[194:197], v[210:213], v[112:115]
	v_mfma_f32_16x16x32_bf16 v[108:111], v[186:189], v[218:221], v[108:111]
	v_mfma_f32_16x16x32_bf16 v[104:107], v[194:197], v[218:221], v[104:107]
	v_mfma_f32_16x16x32_bf16 v[100:103], v[186:189], v[226:229], v[100:103]
	v_mfma_f32_16x16x32_bf16 v[96:99], v[194:197], v[226:229], v[96:99]
	v_mfma_f32_16x16x32_bf16 v[124:127], v[190:193], v[206:209], v[124:127]
	v_mfma_f32_16x16x32_bf16 v[120:123], v[198:201], v[206:209], v[120:123]
	v_mfma_f32_16x16x32_bf16 v[116:119], v[190:193], v[214:217], v[116:119]
	v_mfma_f32_16x16x32_bf16 v[112:115], v[198:201], v[214:217], v[112:115]
	v_mfma_f32_16x16x32_bf16 v[108:111], v[190:193], v[222:225], v[108:111]
	v_mfma_f32_16x16x32_bf16 v[104:107], v[198:201], v[222:225], v[104:107]
	v_mfma_f32_16x16x32_bf16 v[100:103], v[190:193], v[230:233], v[100:103]
	v_mfma_f32_16x16x32_bf16 v[96:99], v[198:201], v[230:233], v[96:99]
	s_setprio 0
	s_barrier
	s_add_i32 s46, s63, s0
	v_lshl_add_u64 v[234:235], v[234:235], 0, s[24:25]
	s_mov_b32 m0, s46
	ds_read_b128 v[202:205], v165 offset:49152
	ds_read_b128 v[206:209], v165 offset:50176
	ds_read_b128 v[210:213], v165 offset:51200
	ds_read_b128 v[214:217], v165 offset:52224
	ds_read_b128 v[218:221], v165 offset:53248
	ds_read_b128 v[222:225], v165 offset:54272
	ds_read_b128 v[226:229], v165 offset:55296
	ds_read_b128 v[230:233], v165 offset:56320
	global_load_lds_dwordx4 v[234:235], off
	s_add_i32 m0, s46, 0x2000
	s_add_u32 s44, s44, 0x80080
	v_lshl_add_u64 v[234:235], v[236:237], 0, s[24:25]
	s_addc_u32 s45, s45, 0
	s_add_i32 s46, s64, s0
	global_load_lds_dwordx4 v[234:235], off
	v_lshl_add_u64 v[234:235], s[44:45], 0, v[136:137]
	s_mov_b32 m0, s46
	v_lshl_add_u64 v[154:155], v[154:155], 0, s[24:25]
	global_load_lds_dwordx4 v[234:235], off
	v_lshl_add_u64 v[234:235], s[44:45], 0, v[138:139]
	s_add_i32 m0, s46, 0x2000
	s_nop 0
	global_load_lds_dwordx4 v[234:235], off
	v_lshl_add_u64 v[234:235], v[238:239], 0, s[24:25]
	s_mov_b32 m0, s49
	s_nop 0
	global_load_lds_dwordx4 v[234:235], off
	s_mov_b32 m0, s51
	s_nop 0
	global_load_lds_dwordx4 v[154:155], off
	s_waitcnt vmcnt(8)
	s_waitcnt lgkmcnt(0)
	s_barrier
	s_setprio 1
	s_waitcnt lgkmcnt(0)
	v_mfma_f32_16x16x32_bf16 v[28:31], v[170:173], v[202:205], v[28:31]
	v_mfma_f32_16x16x32_bf16 v[24:27], v[178:181], v[202:205], v[24:27]
	v_mfma_f32_16x16x32_bf16 v[20:23], v[170:173], v[210:213], v[20:23]
	v_mfma_f32_16x16x32_bf16 v[16:19], v[178:181], v[210:213], v[16:19]
	v_mfma_f32_16x16x32_bf16 v[12:15], v[170:173], v[218:221], v[12:15]
	v_mfma_f32_16x16x32_bf16 v[8:11], v[178:181], v[218:221], v[8:11]
	v_mfma_f32_16x16x32_bf16 v[4:7], v[170:173], v[226:229], v[4:7]
	v_mfma_f32_16x16x32_bf16 v[0:3], v[178:181], v[226:229], v[0:3]
	v_mfma_f32_16x16x32_bf16 v[28:31], v[174:177], v[206:209], v[28:31]
	v_mfma_f32_16x16x32_bf16 v[24:27], v[182:185], v[206:209], v[24:27]
	v_mfma_f32_16x16x32_bf16 v[20:23], v[174:177], v[214:217], v[20:23]
	v_mfma_f32_16x16x32_bf16 v[16:19], v[182:185], v[214:217], v[16:19]
	v_mfma_f32_16x16x32_bf16 v[12:15], v[174:177], v[222:225], v[12:15]
	v_mfma_f32_16x16x32_bf16 v[8:11], v[182:185], v[222:225], v[8:11]
	v_mfma_f32_16x16x32_bf16 v[4:7], v[174:177], v[230:233], v[4:7]
	v_mfma_f32_16x16x32_bf16 v[0:3], v[182:185], v[230:233], v[0:3]
	s_setprio 0
	s_setprio 1
	v_mfma_f32_16x16x32_bf16 v[92:95], v[186:189], v[202:205], v[92:95]
	v_mfma_f32_16x16x32_bf16 v[88:91], v[194:197], v[202:205], v[88:91]
	v_mfma_f32_16x16x32_bf16 v[84:87], v[186:189], v[210:213], v[84:87]
	v_mfma_f32_16x16x32_bf16 v[80:83], v[194:197], v[210:213], v[80:83]
	v_mfma_f32_16x16x32_bf16 v[72:75], v[186:189], v[218:221], v[72:75]
	v_mfma_f32_16x16x32_bf16 v[76:79], v[194:197], v[218:221], v[76:79]
	v_mfma_f32_16x16x32_bf16 v[64:67], v[186:189], v[226:229], v[64:67]
	v_mfma_f32_16x16x32_bf16 v[68:71], v[194:197], v[226:229], v[68:71]
	v_mfma_f32_16x16x32_bf16 v[92:95], v[190:193], v[206:209], v[92:95]
	v_mfma_f32_16x16x32_bf16 v[88:91], v[198:201], v[206:209], v[88:91]
	v_mfma_f32_16x16x32_bf16 v[84:87], v[190:193], v[214:217], v[84:87]
	v_mfma_f32_16x16x32_bf16 v[80:83], v[198:201], v[214:217], v[80:83]
	v_mfma_f32_16x16x32_bf16 v[72:75], v[190:193], v[222:225], v[72:75]
	v_mfma_f32_16x16x32_bf16 v[76:79], v[198:201], v[222:225], v[76:79]
	v_mfma_f32_16x16x32_bf16 v[64:67], v[190:193], v[230:233], v[64:67]
	v_mfma_f32_16x16x32_bf16 v[68:71], v[198:201], v[230:233], v[68:71]
	s_setprio 0
	s_add_i32 s62, s62, 2
	s_add_u32 s10, s10, 0x100
	s_addc_u32 s11, s11, 0
	s_cmp_gt_u32 s62, 29
	s_barrier
	s_cbranch_scc0 .LBB0_1571
	s_and_b64 vcc, exec, s[26:27]
	s_cbranch_vccnz .LBB0_1575
	v_lshl_add_u32 v150, s61, 8, v160
	s_cmp_lg_u32 s12, 46
	s_mov_b64 s[10:11], -1
	s_cbranch_scc1 .LBB0_1576

.LBB0_2279:
	s_add_i32 s65, s30, 2
	s_add_u32 s31, s24, s28
	s_addc_u32 s34, s25, s29
	v_add_u32_e32 v131, s46, v152
	s_add_u32 s66, s31, 0x100
	ds_read_b128 v[160:163], v131
	ds_read_b128 v[164:167], v131 offset:1024
	ds_read_b128 v[168:171], v131 offset:2048
	ds_read_b128 v[172:175], v131 offset:3072
	v_add_u32_e32 v131, s47, v152
	s_addc_u32 s34, s34, 0
	ds_read_b128 v[176:179], v131
	ds_read_b128 v[180:183], v131 offset:1024
	ds_read_b128 v[184:187], v131 offset:2048
	ds_read_b128 v[188:191], v131 offset:3072
	s_add_u32 s67, s63, s28
	s_addc_u32 s68, s64, s29
	s_cmp_eq_u32 s62, s30
	s_cselect_b64 vcc, -1, 0
	s_and_b64 s[30:31], vcc, exec
	s_cselect_b32 s30, s59, s67
	v_cndmask_b32_e32 v136, v128, v156, vcc
	s_cselect_b32 s35, s60, s34
	s_cselect_b32 s34, s61, s66
	v_cndmask_b32_e32 v129, v138, v158, vcc
	v_cndmask_b32_e32 v224, v130, v157, vcc
	v_cndmask_b32_e32 v131, v140, v159, vcc
	s_cselect_b32 s31, s19, s68
	v_lshl_add_u64 v[226:227], v[146:147], 0, s[28:29]
	s_add_i32 m0, s36, 0xc000
	ds_read_b128 v[192:195], v155
	ds_read_b128 v[196:199], v155 offset:1024
	ds_read_b128 v[200:203], v155 offset:2048
	ds_read_b128 v[204:207], v155 offset:3072
	ds_read_b128 v[208:211], v155 offset:4096
	ds_read_b128 v[212:215], v155 offset:5120
	ds_read_b128 v[216:219], v155 offset:6144
	ds_read_b128 v[220:223], v155 offset:7168
	global_load_lds_dwordx4 v[226:227], off
	v_lshl_add_u64 v[226:227], v[142:143], 0, s[28:29]
	s_add_i32 m0, s36, 0xe000
	s_nop 0
	global_load_lds_dwordx4 v[226:227], off
	s_waitcnt vmcnt(8)
	s_waitcnt lgkmcnt(0)
	s_barrier
	s_setprio 1
	s_waitcnt lgkmcnt(0)
	v_mfma_f32_16x16x32_bf16 v[108:111], v[160:163], v[192:195], v[108:111]
	v_mfma_f32_16x16x32_bf16 v[104:107], v[168:171], v[192:195], v[104:107]
	v_mfma_f32_16x16x32_bf16 v[100:103], v[160:163], v[200:203], v[100:103]
	v_mfma_f32_16x16x32_bf16 v[96:99], v[168:171], v[200:203], v[96:99]
	v_mfma_f32_16x16x32_bf16 v[92:95], v[160:163], v[208:211], v[92:95]
	v_mfma_f32_16x16x32_bf16 v[88:91], v[168:171], v[208:211], v[88:91]
	v_mfma_f32_16x16x32_bf16 v[84:87], v[160:163], v[216:219], v[84:87]
	v_mfma_f32_16x16x32_bf16 v[80:83], v[168:171], v[216:219], v[80:83]
	v_mfma_f32_16x16x32_bf16 v[108:111], v[164:167], v[196:199], v[108:111]
	v_mfma_f32_16x16x32_bf16 v[104:107], v[172:175], v[196:199], v[104:107]
	v_mfma_f32_16x16x32_bf16 v[100:103], v[164:167], v[204:207], v[100:103]
	v_mfma_f32_16x16x32_bf16 v[96:99], v[172:175], v[204:207], v[96:99]
	v_mfma_f32_16x16x32_bf16 v[92:95], v[164:167], v[212:215], v[92:95]
	v_mfma_f32_16x16x32_bf16 v[88:91], v[172:175], v[212:215], v[88:91]
	v_mfma_f32_16x16x32_bf16 v[84:87], v[164:167], v[220:223], v[84:87]
	v_mfma_f32_16x16x32_bf16 v[80:83], v[172:175], v[220:223], v[80:83]
	s_setprio 0
	s_setprio 1
	v_mfma_f32_16x16x32_bf16 v[76:79], v[176:179], v[192:195], v[76:79]
	v_mfma_f32_16x16x32_bf16 v[72:75], v[184:187], v[192:195], v[72:75]
	v_mfma_f32_16x16x32_bf16 v[68:71], v[176:179], v[200:203], v[68:71]
	v_mfma_f32_16x16x32_bf16 v[64:67], v[184:187], v[200:203], v[64:67]
	v_mfma_f32_16x16x32_bf16 v[60:63], v[176:179], v[208:211], v[60:63]
	v_mfma_f32_16x16x32_bf16 v[56:59], v[184:187], v[208:211], v[56:59]
	v_mfma_f32_16x16x32_bf16 v[52:55], v[176:179], v[216:219], v[52:55]
	v_mfma_f32_16x16x32_bf16 v[48:51], v[184:187], v[216:219], v[48:51]
	v_mfma_f32_16x16x32_bf16 v[76:79], v[180:183], v[196:199], v[76:79]
	v_mfma_f32_16x16x32_bf16 v[72:75], v[188:191], v[196:199], v[72:75]
	v_mfma_f32_16x16x32_bf16 v[68:71], v[180:183], v[204:207], v[68:71]
	v_mfma_f32_16x16x32_bf16 v[64:67], v[188:191], v[204:207], v[64:67]
	v_mfma_f32_16x16x32_bf16 v[60:63], v[180:183], v[212:215], v[60:63]
	v_mfma_f32_16x16x32_bf16 v[56:59], v[188:191], v[212:215], v[56:59]
	v_mfma_f32_16x16x32_bf16 v[52:55], v[180:183], v[220:223], v[52:55]
	v_mfma_f32_16x16x32_bf16 v[48:51], v[188:191], v[220:223], v[48:51]
	s_setprio 0
	s_barrier
	s_add_i32 s66, s46, s5
	v_lshl_add_u64 v[226:227], s[30:31], 0, v[132:133]
	s_mov_b32 m0, s66
	ds_read_b128 v[192:195], v155 offset:16384
	ds_read_b128 v[196:199], v155 offset:17408
	ds_read_b128 v[200:203], v155 offset:18432
	ds_read_b128 v[204:207], v155 offset:19456
	ds_read_b128 v[208:211], v155 offset:20480
	ds_read_b128 v[212:215], v155 offset:21504
	ds_read_b128 v[216:219], v155 offset:22528
	ds_read_b128 v[220:223], v155 offset:23552
	global_load_lds_dwordx4 v[226:227], off
	s_add_i32 m0, s66, 0x2000
	s_add_u32 s66, s30, 0x80000
	v_lshl_add_u64 v[228:229], s[30:31], 0, v[134:135]
	s_addc_u32 s67, s31, 0
	s_add_i32 s68, s47, s5
	global_load_lds_dwordx4 v[228:229], off
	v_lshl_add_u64 v[230:231], s[66:67], 0, v[132:133]
	s_mov_b32 m0, s68
	v_mov_b32_e32 v225, v137
	global_load_lds_dwordx4 v[230:231], off
	v_lshl_add_u64 v[230:231], s[66:67], 0, v[134:135]
	s_add_i32 m0, s68, 0x2000
	s_nop 0
	global_load_lds_dwordx4 v[230:231], off
	s_mov_b32 m0, s36
	v_lshl_add_u64 v[230:231], s[34:35], 0, v[136:137]
	global_load_lds_dwordx4 v136, s[34:35]
	s_mov_b32 m0, s37
	s_nop 0
	global_load_lds_dwordx4 v224, s[34:35]
	s_waitcnt vmcnt(8)
	s_waitcnt lgkmcnt(0)
	v_lshl_add_u64 v[224:225], s[34:35], 0, v[224:225]
	s_barrier
	s_setprio 1
	s_waitcnt lgkmcnt(0)
	v_mfma_f32_16x16x32_bf16 v[44:47], v[160:163], v[192:195], v[44:47]
	v_mfma_f32_16x16x32_bf16 v[40:43], v[168:171], v[192:195], v[40:43]
	v_mfma_f32_16x16x32_bf16 v[36:39], v[160:163], v[200:203], v[36:39]
	v_mfma_f32_16x16x32_bf16 v[32:35], v[168:171], v[200:203], v[32:35]
	v_mfma_f32_16x16x32_bf16 v[28:31], v[160:163], v[208:211], v[28:31]
	v_mfma_f32_16x16x32_bf16 v[24:27], v[168:171], v[208:211], v[24:27]
	v_mfma_f32_16x16x32_bf16 v[20:23], v[160:163], v[216:219], v[20:23]
	v_mfma_f32_16x16x32_bf16 v[16:19], v[168:171], v[216:219], v[16:19]
	v_mfma_f32_16x16x32_bf16 v[44:47], v[164:167], v[196:199], v[44:47]
	v_mfma_f32_16x16x32_bf16 v[40:43], v[172:175], v[196:199], v[40:43]
	v_mfma_f32_16x16x32_bf16 v[36:39], v[164:167], v[204:207], v[36:39]
	v_mfma_f32_16x16x32_bf16 v[32:35], v[172:175], v[204:207], v[32:35]
	v_mfma_f32_16x16x32_bf16 v[28:31], v[164:167], v[212:215], v[28:31]
	v_mfma_f32_16x16x32_bf16 v[24:27], v[172:175], v[212:215], v[24:27]
	v_mfma_f32_16x16x32_bf16 v[20:23], v[164:167], v[220:223], v[20:23]
	v_mfma_f32_16x16x32_bf16 v[16:19], v[172:175], v[220:223], v[16:19]
	s_setprio 0
	s_setprio 1
	v_mfma_f32_16x16x32_bf16 v[12:15], v[176:179], v[192:195], v[12:15]
	v_mfma_f32_16x16x32_bf16 v[8:11], v[184:187], v[192:195], v[8:11]
	v_mfma_f32_16x16x32_bf16 v[4:7], v[176:179], v[200:203], v[4:7]
	v_mfma_f32_16x16x32_bf16 v[0:3], v[184:187], v[200:203], v[0:3]
	v_mfma_f32_16x16x32_bf16 v[112:115], v[176:179], v[208:211], v[112:115]
	v_mfma_f32_16x16x32_bf16 v[116:119], v[184:187], v[208:211], v[116:119]
	v_mfma_f32_16x16x32_bf16 v[120:123], v[176:179], v[216:219], v[120:123]
	v_mfma_f32_16x16x32_bf16 v[124:127], v[184:187], v[216:219], v[124:127]
	v_mfma_f32_16x16x32_bf16 v[12:15], v[180:183], v[196:199], v[12:15]
	v_mfma_f32_16x16x32_bf16 v[8:11], v[188:191], v[196:199], v[8:11]
	v_mfma_f32_16x16x32_bf16 v[4:7], v[180:183], v[204:207], v[4:7]
	v_mfma_f32_16x16x32_bf16 v[0:3], v[188:191], v[204:207], v[0:3]
	v_mfma_f32_16x16x32_bf16 v[112:115], v[180:183], v[212:215], v[112:115]
	v_mfma_f32_16x16x32_bf16 v[116:119], v[188:191], v[212:215], v[116:119]
	v_mfma_f32_16x16x32_bf16 v[120:123], v[180:183], v[220:223], v[120:123]
	v_mfma_f32_16x16x32_bf16 v[124:127], v[188:191], v[220:223], v[124:127]
	s_setprio 0
	s_barrier
	s_add_i32 s66, 0, 0x18000
	v_add_u32_e32 v136, s66, v152
	s_add_i32 s67, 0, 0x1c000
	ds_read_b128 v[160:163], v136
	ds_read_b128 v[164:167], v136 offset:1024
	ds_read_b128 v[168:171], v136 offset:2048
	ds_read_b128 v[172:175], v136 offset:3072
	v_add_u32_e32 v136, s67, v152
	ds_read_b128 v[176:179], v136
	ds_read_b128 v[180:183], v136 offset:1024
	ds_read_b128 v[184:187], v136 offset:2048
	ds_read_b128 v[188:191], v136 offset:3072
	s_mov_b32 m0, s38
	ds_read_b128 v[192:195], v155 offset:32768
	ds_read_b128 v[196:199], v155 offset:33792
	ds_read_b128 v[200:203], v155 offset:34816
	ds_read_b128 v[204:207], v155 offset:35840
	ds_read_b128 v[208:211], v155 offset:36864
	ds_read_b128 v[212:215], v155 offset:37888
	ds_read_b128 v[216:219], v155 offset:38912
	ds_read_b128 v[220:223], v155 offset:39936
	global_load_lds_dwordx4 v129, s[34:35]
	s_mov_b32 m0, s39
	s_nop 0
	global_load_lds_dwordx4 v131, s[34:35]
	s_waitcnt vmcnt(8)
	s_waitcnt lgkmcnt(0)
	s_barrier
	s_setprio 1
	s_waitcnt lgkmcnt(0)
	v_mfma_f32_16x16x32_bf16 v[108:111], v[160:163], v[192:195], v[108:111]
	v_mfma_f32_16x16x32_bf16 v[104:107], v[168:171], v[192:195], v[104:107]
	v_mfma_f32_16x16x32_bf16 v[100:103], v[160:163], v[200:203], v[100:103]
	v_mfma_f32_16x16x32_bf16 v[96:99], v[168:171], v[200:203], v[96:99]
	v_mfma_f32_16x16x32_bf16 v[92:95], v[160:163], v[208:211], v[92:95]
	v_mfma_f32_16x16x32_bf16 v[88:91], v[168:171], v[208:211], v[88:91]
	v_mfma_f32_16x16x32_bf16 v[84:87], v[160:163], v[216:219], v[84:87]
	v_mfma_f32_16x16x32_bf16 v[80:83], v[168:171], v[216:219], v[80:83]
	v_mfma_f32_16x16x32_bf16 v[108:111], v[164:167], v[196:199], v[108:111]
	v_mfma_f32_16x16x32_bf16 v[104:107], v[172:175], v[196:199], v[104:107]
	v_mfma_f32_16x16x32_bf16 v[100:103], v[164:167], v[204:207], v[100:103]
	v_mfma_f32_16x16x32_bf16 v[96:99], v[172:175], v[204:207], v[96:99]
	v_mfma_f32_16x16x32_bf16 v[92:95], v[164:167], v[212:215], v[92:95]
	v_mfma_f32_16x16x32_bf16 v[88:91], v[172:175], v[212:215], v[88:91]
	v_mfma_f32_16x16x32_bf16 v[84:87], v[164:167], v[220:223], v[84:87]
	v_mfma_f32_16x16x32_bf16 v[80:83], v[172:175], v[220:223], v[80:83]
	s_setprio 0
	s_setprio 1
	v_mfma_f32_16x16x32_bf16 v[76:79], v[176:179], v[192:195], v[76:79]
	v_mfma_f32_16x16x32_bf16 v[72:75], v[184:187], v[192:195], v[72:75]
	v_mfma_f32_16x16x32_bf16 v[68:71], v[176:179], v[200:203], v[68:71]
	v_mfma_f32_16x16x32_bf16 v[64:67], v[184:187], v[200:203], v[64:67]
	v_mfma_f32_16x16x32_bf16 v[60:63], v[176:179], v[208:211], v[60:63]
	v_mfma_f32_16x16x32_bf16 v[56:59], v[184:187], v[208:211], v[56:59]
	v_mfma_f32_16x16x32_bf16 v[52:55], v[176:179], v[216:219], v[52:55]
	v_mfma_f32_16x16x32_bf16 v[48:51], v[184:187], v[216:219], v[48:51]
	v_mfma_f32_16x16x32_bf16 v[76:79], v[180:183], v[196:199], v[76:79]
	v_mfma_f32_16x16x32_bf16 v[72:75], v[188:191], v[196:199], v[72:75]
	v_mfma_f32_16x16x32_bf16 v[68:71], v[180:183], v[204:207], v[68:71]
	v_mfma_f32_16x16x32_bf16 v[64:67], v[188:191], v[204:207], v[64:67]
	v_mfma_f32_16x16x32_bf16 v[60:63], v[180:183], v[212:215], v[60:63]
	v_mfma_f32_16x16x32_bf16 v[56:59], v[188:191], v[212:215], v[56:59]
	v_mfma_f32_16x16x32_bf16 v[52:55], v[180:183], v[220:223], v[52:55]
	v_mfma_f32_16x16x32_bf16 v[48:51], v[188:191], v[220:223], v[48:51]
	s_setprio 0
	s_barrier
	s_add_i32 s34, s66, s5
	v_lshl_add_u64 v[226:227], v[226:227], 0, s[12:13]
	s_mov_b32 m0, s34
	ds_read_b128 v[192:195], v155 offset:49152
	ds_read_b128 v[196:199], v155 offset:50176
	ds_read_b128 v[200:203], v155 offset:51200
	ds_read_b128 v[204:207], v155 offset:52224
	ds_read_b128 v[208:211], v155 offset:53248
	ds_read_b128 v[212:215], v155 offset:54272
	ds_read_b128 v[216:219], v155 offset:55296
	ds_read_b128 v[220:223], v155 offset:56320
	global_load_lds_dwordx4 v[226:227], off
	s_add_i32 m0, s34, 0x2000
	s_add_u32 s30, s30, 0x80080
	v_lshl_add_u64 v[226:227], v[228:229], 0, s[12:13]
	s_addc_u32 s31, s31, 0
	s_add_i32 s34, s67, s5
	global_load_lds_dwordx4 v[226:227], off
	v_lshl_add_u64 v[226:227], s[30:31], 0, v[132:133]
	s_mov_b32 m0, s34
	v_lshl_add_u64 v[224:225], v[224:225], 0, s[12:13]
	global_load_lds_dwordx4 v[226:227], off
	v_lshl_add_u64 v[226:227], s[30:31], 0, v[134:135]
	s_add_i32 m0, s34, 0x2000
	s_nop 0
	global_load_lds_dwordx4 v[226:227], off
	v_lshl_add_u64 v[226:227], v[230:231], 0, s[12:13]
	s_mov_b32 m0, s42
	s_nop 0
	global_load_lds_dwordx4 v[226:227], off
	s_mov_b32 m0, s43
	s_nop 0
	global_load_lds_dwordx4 v[224:225], off
	s_waitcnt vmcnt(8)
	s_waitcnt lgkmcnt(0)
	s_barrier
	s_setprio 1
	s_waitcnt lgkmcnt(0)
	v_mfma_f32_16x16x32_bf16 v[44:47], v[160:163], v[192:195], v[44:47]
	v_mfma_f32_16x16x32_bf16 v[40:43], v[168:171], v[192:195], v[40:43]
	v_mfma_f32_16x16x32_bf16 v[36:39], v[160:163], v[200:203], v[36:39]
	v_mfma_f32_16x16x32_bf16 v[32:35], v[168:171], v[200:203], v[32:35]
	v_mfma_f32_16x16x32_bf16 v[28:31], v[160:163], v[208:211], v[28:31]
	v_mfma_f32_16x16x32_bf16 v[24:27], v[168:171], v[208:211], v[24:27]
	v_mfma_f32_16x16x32_bf16 v[20:23], v[160:163], v[216:219], v[20:23]
	v_mfma_f32_16x16x32_bf16 v[16:19], v[168:171], v[216:219], v[16:19]
	v_mfma_f32_16x16x32_bf16 v[44:47], v[164:167], v[196:199], v[44:47]
	v_mfma_f32_16x16x32_bf16 v[40:43], v[172:175], v[196:199], v[40:43]
	v_mfma_f32_16x16x32_bf16 v[36:39], v[164:167], v[204:207], v[36:39]
	v_mfma_f32_16x16x32_bf16 v[32:35], v[172:175], v[204:207], v[32:35]
	v_mfma_f32_16x16x32_bf16 v[28:31], v[164:167], v[212:215], v[28:31]
	v_mfma_f32_16x16x32_bf16 v[24:27], v[172:175], v[212:215], v[24:27]
	v_mfma_f32_16x16x32_bf16 v[20:23], v[164:167], v[220:223], v[20:23]
	v_mfma_f32_16x16x32_bf16 v[16:19], v[172:175], v[220:223], v[16:19]
	s_setprio 0
	s_setprio 1
	v_mfma_f32_16x16x32_bf16 v[12:15], v[176:179], v[192:195], v[12:15]
	v_mfma_f32_16x16x32_bf16 v[8:11], v[184:187], v[192:195], v[8:11]
	v_mfma_f32_16x16x32_bf16 v[4:7], v[176:179], v[200:203], v[4:7]
	v_mfma_f32_16x16x32_bf16 v[0:3], v[184:187], v[200:203], v[0:3]
	v_mfma_f32_16x16x32_bf16 v[112:115], v[176:179], v[208:211], v[112:115]
	v_mfma_f32_16x16x32_bf16 v[116:119], v[184:187], v[208:211], v[116:119]
	v_mfma_f32_16x16x32_bf16 v[120:123], v[176:179], v[216:219], v[120:123]
	v_mfma_f32_16x16x32_bf16 v[124:127], v[184:187], v[216:219], v[124:127]
	v_mfma_f32_16x16x32_bf16 v[12:15], v[180:183], v[196:199], v[12:15]
	v_mfma_f32_16x16x32_bf16 v[8:11], v[188:191], v[196:199], v[8:11]
	v_mfma_f32_16x16x32_bf16 v[4:7], v[180:183], v[204:207], v[4:7]
	v_mfma_f32_16x16x32_bf16 v[0:3], v[188:191], v[204:207], v[0:3]
	v_mfma_f32_16x16x32_bf16 v[112:115], v[180:183], v[212:215], v[112:115]
	v_mfma_f32_16x16x32_bf16 v[116:119], v[188:191], v[212:215], v[116:119]
	v_mfma_f32_16x16x32_bf16 v[120:123], v[180:183], v[220:223], v[120:123]
	v_mfma_f32_16x16x32_bf16 v[124:127], v[188:191], v[220:223], v[124:127]
	s_setprio 0
	s_add_u32 s28, s28, 0x100
	s_addc_u32 s29, s29, 0
	s_cmp_ge_i32 s65, s57
	s_mov_b32 s30, s65
	s_barrier
	s_cbranch_scc0 .LBB0_2279
	s_and_b64 vcc, exec, s[14:15]
	s_cbranch_vccz .LBB0_2282
	s_barrier

.LBB0_2355:
	ds_read_b128 v[140:143], v162
	ds_read_b128 v[170:173], v162 offset:1024
	ds_read_b128 v[174:177], v162 offset:2048
	ds_read_b128 v[178:181], v162 offset:3072
	ds_read_b128 v[182:185], v163
	ds_read_b128 v[186:189], v163 offset:1024
	ds_read_b128 v[190:193], v163 offset:2048
	ds_read_b128 v[194:197], v163 offset:3072
	s_add_u32 s42, s38, s8
	s_addc_u32 s43, s39, s9
	s_cmpk_eq_i32 s8, 0x1000
	s_cselect_b64 vcc, -1, 0
	s_and_b64 s[40:41], vcc, exec
	s_cselect_b32 s68, 0, s8
	s_cselect_b32 s67, 0, s9
	s_cselect_b32 s40, s65, s42
	s_cselect_b32 s41, s35, s43
	s_add_u32 s42, s10, s68
	v_cndmask_b32_e32 v150, v128, v165, vcc
	v_cndmask_b32_e32 v129, v132, v167, vcc
	v_cndmask_b32_e32 v230, v130, v166, vcc
	v_cndmask_b32_e32 v131, v134, v168, vcc
	s_addc_u32 s43, s11, s67
	v_lshl_add_u64 v[232:233], v[138:139], 0, s[8:9]
	v_lshl_add_u64 v[232:233], v[232:233], 0, s[24:25]
	s_add_i32 m0, s44, 0xc000
	ds_read_b128 v[198:201], v164
	ds_read_b128 v[202:205], v164 offset:1024
	ds_read_b128 v[206:209], v164 offset:2048
	ds_read_b128 v[210:213], v164 offset:3072
	ds_read_b128 v[214:217], v164 offset:4096
	ds_read_b128 v[218:221], v164 offset:5120
	ds_read_b128 v[222:225], v164 offset:6144
	ds_read_b128 v[226:229], v164 offset:7168
	global_load_lds_dwordx4 v[232:233], off
	v_lshl_add_u64 v[232:233], v[136:137], 0, s[8:9]
	v_lshl_add_u64 v[232:233], v[232:233], 0, s[24:25]
	s_add_i32 m0, s44, 0xe000
	s_nop 0
	global_load_lds_dwordx4 v[232:233], off
	s_waitcnt vmcnt(8)
	s_waitcnt lgkmcnt(0)
	s_barrier
	s_setprio 1
	s_waitcnt lgkmcnt(0)
	v_mfma_f32_16x16x32_bf16 v[124:127], v[140:143], v[198:201], v[124:127]
	v_mfma_f32_16x16x32_bf16 v[120:123], v[174:177], v[198:201], v[120:123]
	v_mfma_f32_16x16x32_bf16 v[116:119], v[140:143], v[206:209], v[116:119]
	v_mfma_f32_16x16x32_bf16 v[112:115], v[174:177], v[206:209], v[112:115]
	v_mfma_f32_16x16x32_bf16 v[108:111], v[140:143], v[214:217], v[108:111]
	v_mfma_f32_16x16x32_bf16 v[100:103], v[174:177], v[214:217], v[100:103]
	v_mfma_f32_16x16x32_bf16 v[92:95], v[140:143], v[222:225], v[92:95]
	v_mfma_f32_16x16x32_bf16 v[84:87], v[174:177], v[222:225], v[84:87]
	v_mfma_f32_16x16x32_bf16 v[124:127], v[170:173], v[202:205], v[124:127]
	v_mfma_f32_16x16x32_bf16 v[120:123], v[178:181], v[202:205], v[120:123]
	v_mfma_f32_16x16x32_bf16 v[116:119], v[170:173], v[210:213], v[116:119]
	v_mfma_f32_16x16x32_bf16 v[112:115], v[178:181], v[210:213], v[112:115]
	v_mfma_f32_16x16x32_bf16 v[108:111], v[170:173], v[218:221], v[108:111]
	v_mfma_f32_16x16x32_bf16 v[100:103], v[178:181], v[218:221], v[100:103]
	v_mfma_f32_16x16x32_bf16 v[92:95], v[170:173], v[226:229], v[92:95]
	v_mfma_f32_16x16x32_bf16 v[84:87], v[178:181], v[226:229], v[84:87]
	s_setprio 0
	s_setprio 1
	v_mfma_f32_16x16x32_bf16 v[104:107], v[182:185], v[198:201], v[104:107]
	v_mfma_f32_16x16x32_bf16 v[96:99], v[190:193], v[198:201], v[96:99]
	v_mfma_f32_16x16x32_bf16 v[88:91], v[182:185], v[206:209], v[88:91]
	v_mfma_f32_16x16x32_bf16 v[80:83], v[190:193], v[206:209], v[80:83]
	v_mfma_f32_16x16x32_bf16 v[76:79], v[182:185], v[214:217], v[76:79]
	v_mfma_f32_16x16x32_bf16 v[72:75], v[190:193], v[214:217], v[72:75]
	v_mfma_f32_16x16x32_bf16 v[68:71], v[182:185], v[222:225], v[68:71]
	v_mfma_f32_16x16x32_bf16 v[64:67], v[190:193], v[222:225], v[64:67]
	v_mfma_f32_16x16x32_bf16 v[104:107], v[186:189], v[202:205], v[104:107]
	v_mfma_f32_16x16x32_bf16 v[96:99], v[194:197], v[202:205], v[96:99]
	v_mfma_f32_16x16x32_bf16 v[88:91], v[186:189], v[210:213], v[88:91]
	v_mfma_f32_16x16x32_bf16 v[80:83], v[194:197], v[210:213], v[80:83]
	v_mfma_f32_16x16x32_bf16 v[76:79], v[186:189], v[218:221], v[76:79]
	v_mfma_f32_16x16x32_bf16 v[72:75], v[194:197], v[218:221], v[72:75]
	v_mfma_f32_16x16x32_bf16 v[68:71], v[186:189], v[226:229], v[68:71]
	v_mfma_f32_16x16x32_bf16 v[64:67], v[194:197], v[226:229], v[64:67]
	s_setprio 0
	s_barrier
	s_add_i32 s67, s53, s5
	v_lshl_add_u64 v[232:233], s[40:41], 0, v[146:147]
	s_mov_b32 m0, s67
	ds_read_b128 v[198:201], v164 offset:16384
	ds_read_b128 v[202:205], v164 offset:17408
	ds_read_b128 v[206:209], v164 offset:18432
	ds_read_b128 v[210:213], v164 offset:19456
	ds_read_b128 v[214:217], v164 offset:20480
	ds_read_b128 v[218:221], v164 offset:21504
	ds_read_b128 v[222:225], v164 offset:22528
	ds_read_b128 v[226:229], v164 offset:23552
	global_load_lds_dwordx4 v[232:233], off
	s_add_i32 m0, s67, 0x2000
	s_add_u32 s68, s40, 0x80000
	v_lshl_add_u64 v[234:235], s[40:41], 0, v[148:149]
	s_addc_u32 s69, s41, 0
	s_add_i32 s67, s55, s5
	global_load_lds_dwordx4 v[234:235], off
	v_lshl_add_u64 v[236:237], s[68:69], 0, v[146:147]
	s_mov_b32 m0, s67
	v_mov_b32_e32 v231, v151
	global_load_lds_dwordx4 v[236:237], off
	v_lshl_add_u64 v[236:237], s[68:69], 0, v[148:149]
	s_add_i32 m0, s67, 0x2000
	s_nop 0
	global_load_lds_dwordx4 v[236:237], off
	s_mov_b32 m0, s44
	v_lshl_add_u64 v[236:237], s[42:43], 0, v[150:151]
	global_load_lds_dwordx4 v150, s[42:43]
	s_mov_b32 m0, s45
	s_nop 0
	global_load_lds_dwordx4 v230, s[42:43]
	s_waitcnt vmcnt(8)
	s_waitcnt lgkmcnt(0)
	v_lshl_add_u64 v[230:231], s[42:43], 0, v[230:231]
	s_barrier
	s_setprio 1
	s_waitcnt lgkmcnt(0)
	v_mfma_f32_16x16x32_bf16 v[60:63], v[140:143], v[198:201], v[60:63]
	v_mfma_f32_16x16x32_bf16 v[56:59], v[174:177], v[198:201], v[56:59]
	v_mfma_f32_16x16x32_bf16 v[44:47], v[140:143], v[206:209], v[44:47]
	v_mfma_f32_16x16x32_bf16 v[36:39], v[174:177], v[206:209], v[36:39]
	v_mfma_f32_16x16x32_bf16 v[20:23], v[140:143], v[214:217], v[20:23]
	v_mfma_f32_16x16x32_bf16 v[12:15], v[174:177], v[214:217], v[12:15]
	v_mfma_f32_16x16x32_bf16 v[4:7], v[140:143], v[222:225], v[4:7]
	v_mfma_f32_16x16x32_bf16 v[0:3], v[174:177], v[222:225], v[0:3]
	v_mfma_f32_16x16x32_bf16 v[60:63], v[170:173], v[202:205], v[60:63]
	v_mfma_f32_16x16x32_bf16 v[56:59], v[178:181], v[202:205], v[56:59]
	v_mfma_f32_16x16x32_bf16 v[44:47], v[170:173], v[210:213], v[44:47]
	v_mfma_f32_16x16x32_bf16 v[36:39], v[178:181], v[210:213], v[36:39]
	v_mfma_f32_16x16x32_bf16 v[20:23], v[170:173], v[218:221], v[20:23]
	v_mfma_f32_16x16x32_bf16 v[12:15], v[178:181], v[218:221], v[12:15]
	v_mfma_f32_16x16x32_bf16 v[4:7], v[170:173], v[226:229], v[4:7]
	v_mfma_f32_16x16x32_bf16 v[0:3], v[178:181], v[226:229], v[0:3]
	s_setprio 0
	s_setprio 1
	v_mfma_f32_16x16x32_bf16 v[40:43], v[182:185], v[198:201], v[40:43]
	v_mfma_f32_16x16x32_bf16 v[32:35], v[190:193], v[198:201], v[32:35]
	v_mfma_f32_16x16x32_bf16 v[16:19], v[182:185], v[206:209], v[16:19]
	v_mfma_f32_16x16x32_bf16 v[8:11], v[190:193], v[206:209], v[8:11]
	v_mfma_f32_16x16x32_bf16 v[48:51], v[182:185], v[214:217], v[48:51]
	v_mfma_f32_16x16x32_bf16 v[52:55], v[190:193], v[214:217], v[52:55]
	v_mfma_f32_16x16x32_bf16 v[24:27], v[182:185], v[222:225], v[24:27]
	v_mfma_f32_16x16x32_bf16 v[28:31], v[190:193], v[222:225], v[28:31]
	v_mfma_f32_16x16x32_bf16 v[40:43], v[186:189], v[202:205], v[40:43]
	v_mfma_f32_16x16x32_bf16 v[32:35], v[194:197], v[202:205], v[32:35]
	v_mfma_f32_16x16x32_bf16 v[16:19], v[186:189], v[210:213], v[16:19]
	v_mfma_f32_16x16x32_bf16 v[8:11], v[194:197], v[210:213], v[8:11]
	v_mfma_f32_16x16x32_bf16 v[48:51], v[186:189], v[218:221], v[48:51]
	v_mfma_f32_16x16x32_bf16 v[52:55], v[194:197], v[218:221], v[52:55]
	v_mfma_f32_16x16x32_bf16 v[24:27], v[186:189], v[226:229], v[24:27]
	v_mfma_f32_16x16x32_bf16 v[28:31], v[194:197], v[226:229], v[28:31]
	s_setprio 0
	s_barrier
	s_add_i32 s67, 0, 0x18000
	v_add_u32_e32 v133, s67, v160
	s_add_i32 s68, 0, 0x1c000
	ds_read_b128 v[140:143], v133
	ds_read_b128 v[170:173], v133 offset:1024
	ds_read_b128 v[174:177], v133 offset:2048
	ds_read_b128 v[178:181], v133 offset:3072
	v_add_u32_e32 v133, s68, v160
	ds_read_b128 v[182:185], v133
	ds_read_b128 v[186:189], v133 offset:1024
	ds_read_b128 v[190:193], v133 offset:2048
	ds_read_b128 v[194:197], v133 offset:3072
	s_mov_b32 m0, s46
	ds_read_b128 v[198:201], v164 offset:32768
	ds_read_b128 v[202:205], v164 offset:33792
	ds_read_b128 v[206:209], v164 offset:34816
	ds_read_b128 v[210:213], v164 offset:35840
	ds_read_b128 v[214:217], v164 offset:36864
	ds_read_b128 v[218:221], v164 offset:37888
	ds_read_b128 v[222:225], v164 offset:38912
	ds_read_b128 v[226:229], v164 offset:39936
	global_load_lds_dwordx4 v129, s[42:43]
	s_mov_b32 m0, s47
	s_nop 0
	global_load_lds_dwordx4 v131, s[42:43]
	s_waitcnt vmcnt(8)
	s_waitcnt lgkmcnt(0)
	s_barrier
	s_setprio 1
	s_waitcnt lgkmcnt(0)
	v_mfma_f32_16x16x32_bf16 v[124:127], v[140:143], v[198:201], v[124:127]
	v_mfma_f32_16x16x32_bf16 v[120:123], v[174:177], v[198:201], v[120:123]
	v_mfma_f32_16x16x32_bf16 v[116:119], v[140:143], v[206:209], v[116:119]
	v_mfma_f32_16x16x32_bf16 v[112:115], v[174:177], v[206:209], v[112:115]
	v_mfma_f32_16x16x32_bf16 v[108:111], v[140:143], v[214:217], v[108:111]
	v_mfma_f32_16x16x32_bf16 v[100:103], v[174:177], v[214:217], v[100:103]
	v_mfma_f32_16x16x32_bf16 v[92:95], v[140:143], v[222:225], v[92:95]
	v_mfma_f32_16x16x32_bf16 v[84:87], v[174:177], v[222:225], v[84:87]
	v_mfma_f32_16x16x32_bf16 v[124:127], v[170:173], v[202:205], v[124:127]
	v_mfma_f32_16x16x32_bf16 v[120:123], v[178:181], v[202:205], v[120:123]
	v_mfma_f32_16x16x32_bf16 v[116:119], v[170:173], v[210:213], v[116:119]
	v_mfma_f32_16x16x32_bf16 v[112:115], v[178:181], v[210:213], v[112:115]
	v_mfma_f32_16x16x32_bf16 v[108:111], v[170:173], v[218:221], v[108:111]
	v_mfma_f32_16x16x32_bf16 v[100:103], v[178:181], v[218:221], v[100:103]
	v_mfma_f32_16x16x32_bf16 v[92:95], v[170:173], v[226:229], v[92:95]
	v_mfma_f32_16x16x32_bf16 v[84:87], v[178:181], v[226:229], v[84:87]
	s_setprio 0
	s_setprio 1
	v_mfma_f32_16x16x32_bf16 v[104:107], v[182:185], v[198:201], v[104:107]
	v_mfma_f32_16x16x32_bf16 v[96:99], v[190:193], v[198:201], v[96:99]
	v_mfma_f32_16x16x32_bf16 v[88:91], v[182:185], v[206:209], v[88:91]
	v_mfma_f32_16x16x32_bf16 v[80:83], v[190:193], v[206:209], v[80:83]
	v_mfma_f32_16x16x32_bf16 v[76:79], v[182:185], v[214:217], v[76:79]
	v_mfma_f32_16x16x32_bf16 v[72:75], v[190:193], v[214:217], v[72:75]
	v_mfma_f32_16x16x32_bf16 v[68:71], v[182:185], v[222:225], v[68:71]
	v_mfma_f32_16x16x32_bf16 v[64:67], v[190:193], v[222:225], v[64:67]
	v_mfma_f32_16x16x32_bf16 v[104:107], v[186:189], v[202:205], v[104:107]
	v_mfma_f32_16x16x32_bf16 v[96:99], v[194:197], v[202:205], v[96:99]
	v_mfma_f32_16x16x32_bf16 v[88:91], v[186:189], v[210:213], v[88:91]
	v_mfma_f32_16x16x32_bf16 v[80:83], v[194:197], v[210:213], v[80:83]
	v_mfma_f32_16x16x32_bf16 v[76:79], v[186:189], v[218:221], v[76:79]
	v_mfma_f32_16x16x32_bf16 v[72:75], v[194:197], v[218:221], v[72:75]
	v_mfma_f32_16x16x32_bf16 v[68:71], v[186:189], v[226:229], v[68:71]
	v_mfma_f32_16x16x32_bf16 v[64:67], v[194:197], v[226:229], v[64:67]
	s_setprio 0
	s_barrier
	s_add_i32 s42, s67, s5
	v_lshl_add_u64 v[232:233], v[232:233], 0, s[20:21]
	s_mov_b32 m0, s42
	ds_read_b128 v[198:201], v164 offset:49152
	ds_read_b128 v[202:205], v164 offset:50176
	ds_read_b128 v[206:209], v164 offset:51200
	ds_read_b128 v[210:213], v164 offset:52224
	ds_read_b128 v[214:217], v164 offset:53248
	ds_read_b128 v[218:221], v164 offset:54272
	ds_read_b128 v[222:225], v164 offset:55296
	ds_read_b128 v[226:229], v164 offset:56320
	global_load_lds_dwordx4 v[232:233], off
	s_add_i32 m0, s42, 0x2000
	s_add_u32 s40, s40, 0x80080
	v_lshl_add_u64 v[232:233], v[234:235], 0, s[20:21]
	s_addc_u32 s41, s41, 0
	s_add_i32 s42, s68, s5
	global_load_lds_dwordx4 v[232:233], off
	v_lshl_add_u64 v[232:233], s[40:41], 0, v[146:147]
	s_mov_b32 m0, s42
	v_lshl_add_u64 v[230:231], v[230:231], 0, s[20:21]
	global_load_lds_dwordx4 v[232:233], off
	v_lshl_add_u64 v[232:233], s[40:41], 0, v[148:149]
	s_add_i32 m0, s42, 0x2000
	s_nop 0
	global_load_lds_dwordx4 v[232:233], off
	v_lshl_add_u64 v[232:233], v[236:237], 0, s[20:21]
	s_mov_b32 m0, s49
	s_nop 0
	global_load_lds_dwordx4 v[232:233], off
	s_mov_b32 m0, s51
	s_nop 0
	global_load_lds_dwordx4 v[230:231], off
	s_waitcnt vmcnt(8)
	s_waitcnt lgkmcnt(0)
	s_barrier
	s_setprio 1
	s_waitcnt lgkmcnt(0)
	v_mfma_f32_16x16x32_bf16 v[60:63], v[140:143], v[198:201], v[60:63]
	v_mfma_f32_16x16x32_bf16 v[56:59], v[174:177], v[198:201], v[56:59]
	v_mfma_f32_16x16x32_bf16 v[44:47], v[140:143], v[206:209], v[44:47]
	v_mfma_f32_16x16x32_bf16 v[36:39], v[174:177], v[206:209], v[36:39]
	v_mfma_f32_16x16x32_bf16 v[20:23], v[140:143], v[214:217], v[20:23]
	v_mfma_f32_16x16x32_bf16 v[12:15], v[174:177], v[214:217], v[12:15]
	v_mfma_f32_16x16x32_bf16 v[4:7], v[140:143], v[222:225], v[4:7]
	v_mfma_f32_16x16x32_bf16 v[0:3], v[174:177], v[222:225], v[0:3]
	v_mfma_f32_16x16x32_bf16 v[60:63], v[170:173], v[202:205], v[60:63]
	v_mfma_f32_16x16x32_bf16 v[56:59], v[178:181], v[202:205], v[56:59]
	v_mfma_f32_16x16x32_bf16 v[44:47], v[170:173], v[210:213], v[44:47]
	v_mfma_f32_16x16x32_bf16 v[36:39], v[178:181], v[210:213], v[36:39]
	v_mfma_f32_16x16x32_bf16 v[20:23], v[170:173], v[218:221], v[20:23]
	v_mfma_f32_16x16x32_bf16 v[12:15], v[178:181], v[218:221], v[12:15]
	v_mfma_f32_16x16x32_bf16 v[4:7], v[170:173], v[226:229], v[4:7]
	v_mfma_f32_16x16x32_bf16 v[0:3], v[178:181], v[226:229], v[0:3]
	s_setprio 0
	s_setprio 1
	v_mfma_f32_16x16x32_bf16 v[40:43], v[182:185], v[198:201], v[40:43]
	v_mfma_f32_16x16x32_bf16 v[32:35], v[190:193], v[198:201], v[32:35]
	v_mfma_f32_16x16x32_bf16 v[16:19], v[182:185], v[206:209], v[16:19]
	v_mfma_f32_16x16x32_bf16 v[8:11], v[190:193], v[206:209], v[8:11]
	v_mfma_f32_16x16x32_bf16 v[48:51], v[182:185], v[214:217], v[48:51]
	v_mfma_f32_16x16x32_bf16 v[52:55], v[190:193], v[214:217], v[52:55]
	v_mfma_f32_16x16x32_bf16 v[24:27], v[182:185], v[222:225], v[24:27]
	v_mfma_f32_16x16x32_bf16 v[28:31], v[190:193], v[222:225], v[28:31]
	v_mfma_f32_16x16x32_bf16 v[40:43], v[186:189], v[202:205], v[40:43]
	v_mfma_f32_16x16x32_bf16 v[32:35], v[194:197], v[202:205], v[32:35]
	v_mfma_f32_16x16x32_bf16 v[16:19], v[186:189], v[210:213], v[16:19]
	v_mfma_f32_16x16x32_bf16 v[8:11], v[194:197], v[210:213], v[8:11]
	v_mfma_f32_16x16x32_bf16 v[48:51], v[186:189], v[218:221], v[48:51]
	v_mfma_f32_16x16x32_bf16 v[52:55], v[194:197], v[218:221], v[52:55]
	v_mfma_f32_16x16x32_bf16 v[24:27], v[186:189], v[226:229], v[24:27]
	v_mfma_f32_16x16x32_bf16 v[28:31], v[194:197], v[226:229], v[28:31]
	s_setprio 0
	s_add_i32 s66, s66, 2
	s_add_u32 s8, s8, 0x100
	s_addc_u32 s9, s9, 0
	s_cmp_gt_u32 s66, 29
	s_barrier
	s_cbranch_scc0 .LBB0_2355
	s_and_b64 vcc, exec, s[22:23]
	s_cbranch_vccz .LBB0_2358
	s_barrier

.LBB0_2750:
	v_add_u32_e32 v163, s48, v143
	ds_read_b128 v[164:167], v163
	ds_read_b128 v[168:171], v163 offset:1024
	ds_read_b128 v[172:175], v163 offset:2048
	ds_read_b128 v[176:179], v163 offset:3072
	v_add_u32_e32 v163, s49, v143
	ds_read_b128 v[180:183], v163
	ds_read_b128 v[184:187], v163 offset:1024
	ds_read_b128 v[188:191], v163 offset:2048
	ds_read_b128 v[192:195], v163 offset:3072
	s_cmpk_eq_i32 s8, 0x1000
	s_cselect_b64 vcc, -1, 0
	s_and_b64 s[40:41], vcc, exec
	s_cselect_b32 s40, 0, s8
	v_lshl_add_u64 v[196:197], v[148:149], 0, s[8:9]
	s_cselect_b32 s41, 0, s9
	s_add_u32 s40, s18, s40
	v_cndmask_b32_e32 v132, v146, v158, vcc
	v_cndmask_b32_e32 v139, v140, v160, vcc
	v_cndmask_b32_e32 v228, v142, v159, vcc
	v_cndmask_b32_e32 v141, v138, v161, vcc
	v_cndmask_b32_e32 v230, v196, v162, vcc
	v_cndmask_b32_e32 v231, v197, v135, vcc
	s_addc_u32 s41, s19, s41
	v_lshl_add_u64 v[232:233], v[152:153], 0, s[8:9]
	s_mov_b32 m0, s52
	v_lshl_add_u64 v[232:233], v[232:233], 0, s[36:37]
	ds_read_b128 v[196:199], v157
	ds_read_b128 v[200:203], v157 offset:1024
	ds_read_b128 v[204:207], v157 offset:2048
	ds_read_b128 v[208:211], v157 offset:3072
	ds_read_b128 v[212:215], v157 offset:4096
	ds_read_b128 v[216:219], v157 offset:5120
	ds_read_b128 v[220:223], v157 offset:6144
	ds_read_b128 v[224:227], v157 offset:7168
	global_load_lds_dwordx4 v[232:233], off
	v_lshl_add_u64 v[232:233], v[150:151], 0, s[8:9]
	v_lshl_add_u64 v[232:233], v[232:233], 0, s[36:37]
	s_mov_b32 m0, s53
	s_nop 0
	global_load_lds_dwordx4 v[232:233], off
	s_waitcnt vmcnt(8)
	s_waitcnt lgkmcnt(0)
	s_barrier
	s_setprio 1
	s_waitcnt lgkmcnt(0)
	v_mfma_f32_16x16x32_bf16 v[124:127], v[164:167], v[196:199], v[124:127]
	v_mfma_f32_16x16x32_bf16 v[120:123], v[172:175], v[196:199], v[120:123]
	v_mfma_f32_16x16x32_bf16 v[108:111], v[164:167], v[204:207], v[108:111]
	v_mfma_f32_16x16x32_bf16 v[104:107], v[172:175], v[204:207], v[104:107]
	v_mfma_f32_16x16x32_bf16 v[92:95], v[164:167], v[212:215], v[92:95]
	v_mfma_f32_16x16x32_bf16 v[88:91], v[172:175], v[212:215], v[88:91]
	v_mfma_f32_16x16x32_bf16 v[76:79], v[164:167], v[220:223], v[76:79]
	v_mfma_f32_16x16x32_bf16 v[72:75], v[172:175], v[220:223], v[72:75]
	v_mfma_f32_16x16x32_bf16 v[124:127], v[168:171], v[200:203], v[124:127]
	v_mfma_f32_16x16x32_bf16 v[120:123], v[176:179], v[200:203], v[120:123]
	v_mfma_f32_16x16x32_bf16 v[108:111], v[168:171], v[208:211], v[108:111]
	v_mfma_f32_16x16x32_bf16 v[104:107], v[176:179], v[208:211], v[104:107]
	v_mfma_f32_16x16x32_bf16 v[92:95], v[168:171], v[216:219], v[92:95]
	v_mfma_f32_16x16x32_bf16 v[88:91], v[176:179], v[216:219], v[88:91]
	v_mfma_f32_16x16x32_bf16 v[76:79], v[168:171], v[224:227], v[76:79]
	v_mfma_f32_16x16x32_bf16 v[72:75], v[176:179], v[224:227], v[72:75]
	s_setprio 0
	s_setprio 1
	v_mfma_f32_16x16x32_bf16 v[116:119], v[180:183], v[196:199], v[116:119]
	v_mfma_f32_16x16x32_bf16 v[112:115], v[188:191], v[196:199], v[112:115]
	v_mfma_f32_16x16x32_bf16 v[100:103], v[180:183], v[204:207], v[100:103]
	v_mfma_f32_16x16x32_bf16 v[96:99], v[188:191], v[204:207], v[96:99]
	v_mfma_f32_16x16x32_bf16 v[84:87], v[180:183], v[212:215], v[84:87]
	v_mfma_f32_16x16x32_bf16 v[80:83], v[188:191], v[212:215], v[80:83]
	v_mfma_f32_16x16x32_bf16 v[68:71], v[180:183], v[220:223], v[68:71]
	v_mfma_f32_16x16x32_bf16 v[64:67], v[188:191], v[220:223], v[64:67]
	v_mfma_f32_16x16x32_bf16 v[116:119], v[184:187], v[200:203], v[116:119]
	v_mfma_f32_16x16x32_bf16 v[112:115], v[192:195], v[200:203], v[112:115]
	v_mfma_f32_16x16x32_bf16 v[100:103], v[184:187], v[208:211], v[100:103]
	v_mfma_f32_16x16x32_bf16 v[96:99], v[192:195], v[208:211], v[96:99]
	v_mfma_f32_16x16x32_bf16 v[84:87], v[184:187], v[216:219], v[84:87]
	v_mfma_f32_16x16x32_bf16 v[80:83], v[192:195], v[216:219], v[80:83]
	v_mfma_f32_16x16x32_bf16 v[68:71], v[184:187], v[224:227], v[68:71]
	v_mfma_f32_16x16x32_bf16 v[64:67], v[192:195], v[224:227], v[64:67]
	s_setprio 0
	s_barrier
	s_mov_b32 m0, s55
	v_lshl_add_u64 v[232:233], v[230:231], 0, v[128:129]
	ds_read_b128 v[196:199], v157 offset:16384
	ds_read_b128 v[200:203], v157 offset:17408
	ds_read_b128 v[204:207], v157 offset:18432
	ds_read_b128 v[208:211], v157 offset:19456
	ds_read_b128 v[212:215], v157 offset:20480
	ds_read_b128 v[216:219], v157 offset:21504
	ds_read_b128 v[220:223], v157 offset:22528
	ds_read_b128 v[224:227], v157 offset:23552
	global_load_lds_dwordx4 v[232:233], off
	v_lshl_add_u64 v[234:235], v[230:231], 0, v[130:131]
	s_mov_b32 m0, s57
	v_lshl_add_u64 v[236:237], v[230:231], 0, s[24:25]
	global_load_lds_dwordx4 v[234:235], off
	v_lshl_add_u64 v[238:239], v[236:237], 0, v[128:129]
	s_mov_b32 m0, s59
	v_lshl_add_u64 v[236:237], v[236:237], 0, v[130:131]
	global_load_lds_dwordx4 v[238:239], off
	s_mov_b32 m0, s60
	v_mov_b32_e32 v229, v133
	global_load_lds_dwordx4 v[236:237], off
	s_mov_b32 m0, s1
	v_lshl_add_u64 v[236:237], s[40:41], 0, v[132:133]
	global_load_lds_dwordx4 v132, s[40:41]
	s_mov_b32 m0, s22
	s_nop 0
	global_load_lds_dwordx4 v228, s[40:41]
	s_waitcnt vmcnt(8)
	s_waitcnt lgkmcnt(0)
	v_lshl_add_u64 v[228:229], s[40:41], 0, v[228:229]
	s_barrier
	s_setprio 1
	s_waitcnt lgkmcnt(0)
	v_mfma_f32_16x16x32_bf16 v[60:63], v[164:167], v[196:199], v[60:63]
	v_mfma_f32_16x16x32_bf16 v[56:59], v[172:175], v[196:199], v[56:59]
	v_mfma_f32_16x16x32_bf16 v[44:47], v[164:167], v[204:207], v[44:47]
	v_mfma_f32_16x16x32_bf16 v[36:39], v[172:175], v[204:207], v[36:39]
	v_mfma_f32_16x16x32_bf16 v[20:23], v[164:167], v[212:215], v[20:23]
	v_mfma_f32_16x16x32_bf16 v[8:11], v[172:175], v[212:215], v[8:11]
	v_mfma_f32_16x16x32_bf16 v[4:7], v[164:167], v[220:223], v[4:7]
	v_mfma_f32_16x16x32_bf16 v[0:3], v[172:175], v[220:223], v[0:3]
	v_mfma_f32_16x16x32_bf16 v[60:63], v[168:171], v[200:203], v[60:63]
	v_mfma_f32_16x16x32_bf16 v[56:59], v[176:179], v[200:203], v[56:59]
	v_mfma_f32_16x16x32_bf16 v[44:47], v[168:171], v[208:211], v[44:47]
	v_mfma_f32_16x16x32_bf16 v[36:39], v[176:179], v[208:211], v[36:39]
	v_mfma_f32_16x16x32_bf16 v[20:23], v[168:171], v[216:219], v[20:23]
	v_mfma_f32_16x16x32_bf16 v[8:11], v[176:179], v[216:219], v[8:11]
	v_mfma_f32_16x16x32_bf16 v[4:7], v[168:171], v[224:227], v[4:7]
	v_mfma_f32_16x16x32_bf16 v[0:3], v[176:179], v[224:227], v[0:3]
	s_setprio 0
	s_setprio 1
	v_mfma_f32_16x16x32_bf16 v[52:55], v[180:183], v[196:199], v[52:55]
	v_mfma_f32_16x16x32_bf16 v[48:51], v[188:191], v[196:199], v[48:51]
	v_mfma_f32_16x16x32_bf16 v[28:31], v[180:183], v[204:207], v[28:31]
	v_mfma_f32_16x16x32_bf16 v[24:27], v[188:191], v[204:207], v[24:27]
	v_mfma_f32_16x16x32_bf16 v[40:43], v[180:183], v[212:215], v[40:43]
	v_mfma_f32_16x16x32_bf16 v[32:35], v[188:191], v[212:215], v[32:35]
	v_mfma_f32_16x16x32_bf16 v[16:19], v[180:183], v[220:223], v[16:19]
	v_mfma_f32_16x16x32_bf16 v[12:15], v[188:191], v[220:223], v[12:15]
	v_mfma_f32_16x16x32_bf16 v[52:55], v[184:187], v[200:203], v[52:55]
	v_mfma_f32_16x16x32_bf16 v[48:51], v[192:195], v[200:203], v[48:51]
	v_mfma_f32_16x16x32_bf16 v[28:31], v[184:187], v[208:211], v[28:31]
	v_mfma_f32_16x16x32_bf16 v[24:27], v[192:195], v[208:211], v[24:27]
	v_mfma_f32_16x16x32_bf16 v[40:43], v[184:187], v[216:219], v[40:43]
	v_mfma_f32_16x16x32_bf16 v[32:35], v[192:195], v[216:219], v[32:35]
	v_mfma_f32_16x16x32_bf16 v[16:19], v[184:187], v[224:227], v[16:19]
	v_mfma_f32_16x16x32_bf16 v[12:15], v[192:195], v[224:227], v[12:15]
	s_setprio 0
	s_barrier
	v_add_u32_e32 v132, s61, v143
	s_add_i32 s51, 0, 0x1c000
	ds_read_b128 v[164:167], v132
	ds_read_b128 v[168:171], v132 offset:1024
	ds_read_b128 v[172:175], v132 offset:2048
	ds_read_b128 v[176:179], v132 offset:3072
	v_add_u32_e32 v132, s51, v143
	ds_read_b128 v[180:183], v132
	ds_read_b128 v[184:187], v132 offset:1024
	ds_read_b128 v[188:191], v132 offset:2048
	ds_read_b128 v[192:195], v132 offset:3072
	s_mov_b32 m0, s42
	ds_read_b128 v[196:199], v157 offset:32768
	ds_read_b128 v[200:203], v157 offset:33792
	ds_read_b128 v[204:207], v157 offset:34816
	ds_read_b128 v[208:211], v157 offset:35840
	ds_read_b128 v[212:215], v157 offset:36864
	ds_read_b128 v[216:219], v157 offset:37888
	ds_read_b128 v[220:223], v157 offset:38912
	ds_read_b128 v[224:227], v157 offset:39936
	global_load_lds_dwordx4 v139, s[40:41]
	s_mov_b32 m0, s43
	s_nop 0
	global_load_lds_dwordx4 v141, s[40:41]
	s_waitcnt vmcnt(8)
	s_waitcnt lgkmcnt(0)
	s_barrier
	s_setprio 1
	s_waitcnt lgkmcnt(0)
	v_mfma_f32_16x16x32_bf16 v[124:127], v[164:167], v[196:199], v[124:127]
	v_mfma_f32_16x16x32_bf16 v[120:123], v[172:175], v[196:199], v[120:123]
	v_mfma_f32_16x16x32_bf16 v[108:111], v[164:167], v[204:207], v[108:111]
	v_mfma_f32_16x16x32_bf16 v[104:107], v[172:175], v[204:207], v[104:107]
	v_mfma_f32_16x16x32_bf16 v[92:95], v[164:167], v[212:215], v[92:95]
	v_mfma_f32_16x16x32_bf16 v[88:91], v[172:175], v[212:215], v[88:91]
	v_mfma_f32_16x16x32_bf16 v[76:79], v[164:167], v[220:223], v[76:79]
	v_mfma_f32_16x16x32_bf16 v[72:75], v[172:175], v[220:223], v[72:75]
	v_mfma_f32_16x16x32_bf16 v[124:127], v[168:171], v[200:203], v[124:127]
	v_mfma_f32_16x16x32_bf16 v[120:123], v[176:179], v[200:203], v[120:123]
	v_mfma_f32_16x16x32_bf16 v[108:111], v[168:171], v[208:211], v[108:111]
	v_mfma_f32_16x16x32_bf16 v[104:107], v[176:179], v[208:211], v[104:107]
	v_mfma_f32_16x16x32_bf16 v[92:95], v[168:171], v[216:219], v[92:95]
	v_mfma_f32_16x16x32_bf16 v[88:91], v[176:179], v[216:219], v[88:91]
	v_mfma_f32_16x16x32_bf16 v[76:79], v[168:171], v[224:227], v[76:79]
	v_mfma_f32_16x16x32_bf16 v[72:75], v[176:179], v[224:227], v[72:75]
	s_setprio 0
	s_setprio 1
	v_mfma_f32_16x16x32_bf16 v[116:119], v[180:183], v[196:199], v[116:119]
	v_mfma_f32_16x16x32_bf16 v[112:115], v[188:191], v[196:199], v[112:115]
	v_mfma_f32_16x16x32_bf16 v[100:103], v[180:183], v[204:207], v[100:103]
	v_mfma_f32_16x16x32_bf16 v[96:99], v[188:191], v[204:207], v[96:99]
	v_mfma_f32_16x16x32_bf16 v[84:87], v[180:183], v[212:215], v[84:87]
	v_mfma_f32_16x16x32_bf16 v[80:83], v[188:191], v[212:215], v[80:83]
	v_mfma_f32_16x16x32_bf16 v[68:71], v[180:183], v[220:223], v[68:71]
	v_mfma_f32_16x16x32_bf16 v[64:67], v[188:191], v[220:223], v[64:67]
	v_mfma_f32_16x16x32_bf16 v[116:119], v[184:187], v[200:203], v[116:119]
	v_mfma_f32_16x16x32_bf16 v[112:115], v[192:195], v[200:203], v[112:115]
	v_mfma_f32_16x16x32_bf16 v[100:103], v[184:187], v[208:211], v[100:103]
	v_mfma_f32_16x16x32_bf16 v[96:99], v[192:195], v[208:211], v[96:99]
	v_mfma_f32_16x16x32_bf16 v[84:87], v[184:187], v[216:219], v[84:87]
	v_mfma_f32_16x16x32_bf16 v[80:83], v[192:195], v[216:219], v[80:83]
	v_mfma_f32_16x16x32_bf16 v[68:71], v[184:187], v[224:227], v[68:71]
	v_mfma_f32_16x16x32_bf16 v[64:67], v[192:195], v[224:227], v[64:67]
	s_setprio 0
	s_barrier
	s_add_i32 s40, s61, s0
	v_lshl_add_u64 v[232:233], v[232:233], 0, s[28:29]
	s_mov_b32 m0, s40
	ds_read_b128 v[196:199], v157 offset:49152
	ds_read_b128 v[200:203], v157 offset:50176
	ds_read_b128 v[204:207], v157 offset:51200
	ds_read_b128 v[208:211], v157 offset:52224
	ds_read_b128 v[212:215], v157 offset:53248
	ds_read_b128 v[216:219], v157 offset:54272
	ds_read_b128 v[220:223], v157 offset:55296
	ds_read_b128 v[224:227], v157 offset:56320
	global_load_lds_dwordx4 v[232:233], off
	v_lshl_add_u64 v[232:233], v[234:235], 0, s[28:29]
	s_add_i32 m0, s40, 0x2000
	v_lshl_add_u64 v[230:231], v[230:231], 0, s[30:31]
	s_add_i32 s40, s51, s0
	global_load_lds_dwordx4 v[232:233], off
	v_lshl_add_u64 v[232:233], v[230:231], 0, v[128:129]
	s_mov_b32 m0, s40
	v_lshl_add_u64 v[230:231], v[230:231], 0, v[130:131]
	global_load_lds_dwordx4 v[232:233], off
	s_add_i32 m0, s40, 0x2000
	v_lshl_add_u64 v[228:229], v[228:229], 0, s[28:29]
	global_load_lds_dwordx4 v[230:231], off
	v_lshl_add_u64 v[230:231], v[236:237], 0, s[28:29]
	s_mov_b32 m0, s46
	s_nop 0
	global_load_lds_dwordx4 v[230:231], off
	s_mov_b32 m0, s47
	s_nop 0
	global_load_lds_dwordx4 v[228:229], off
	s_waitcnt vmcnt(8)
	s_waitcnt lgkmcnt(0)
	s_barrier
	s_setprio 1
	s_waitcnt lgkmcnt(0)
	v_mfma_f32_16x16x32_bf16 v[60:63], v[164:167], v[196:199], v[60:63]
	v_mfma_f32_16x16x32_bf16 v[56:59], v[172:175], v[196:199], v[56:59]
	v_mfma_f32_16x16x32_bf16 v[44:47], v[164:167], v[204:207], v[44:47]
	v_mfma_f32_16x16x32_bf16 v[36:39], v[172:175], v[204:207], v[36:39]
	v_mfma_f32_16x16x32_bf16 v[20:23], v[164:167], v[212:215], v[20:23]
	v_mfma_f32_16x16x32_bf16 v[8:11], v[172:175], v[212:215], v[8:11]
	v_mfma_f32_16x16x32_bf16 v[4:7], v[164:167], v[220:223], v[4:7]
	v_mfma_f32_16x16x32_bf16 v[0:3], v[172:175], v[220:223], v[0:3]
	v_mfma_f32_16x16x32_bf16 v[60:63], v[168:171], v[200:203], v[60:63]
	v_mfma_f32_16x16x32_bf16 v[56:59], v[176:179], v[200:203], v[56:59]
	v_mfma_f32_16x16x32_bf16 v[44:47], v[168:171], v[208:211], v[44:47]
	v_mfma_f32_16x16x32_bf16 v[36:39], v[176:179], v[208:211], v[36:39]
	v_mfma_f32_16x16x32_bf16 v[20:23], v[168:171], v[216:219], v[20:23]
	v_mfma_f32_16x16x32_bf16 v[8:11], v[176:179], v[216:219], v[8:11]
	v_mfma_f32_16x16x32_bf16 v[4:7], v[168:171], v[224:227], v[4:7]
	v_mfma_f32_16x16x32_bf16 v[0:3], v[176:179], v[224:227], v[0:3]
	s_setprio 0
	s_setprio 1
	v_mfma_f32_16x16x32_bf16 v[52:55], v[180:183], v[196:199], v[52:55]
	v_mfma_f32_16x16x32_bf16 v[48:51], v[188:191], v[196:199], v[48:51]
	v_mfma_f32_16x16x32_bf16 v[28:31], v[180:183], v[204:207], v[28:31]
	v_mfma_f32_16x16x32_bf16 v[24:27], v[188:191], v[204:207], v[24:27]
	v_mfma_f32_16x16x32_bf16 v[40:43], v[180:183], v[212:215], v[40:43]
	v_mfma_f32_16x16x32_bf16 v[32:35], v[188:191], v[212:215], v[32:35]
	v_mfma_f32_16x16x32_bf16 v[16:19], v[180:183], v[220:223], v[16:19]
	v_mfma_f32_16x16x32_bf16 v[12:15], v[188:191], v[220:223], v[12:15]
	v_mfma_f32_16x16x32_bf16 v[52:55], v[184:187], v[200:203], v[52:55]
	v_mfma_f32_16x16x32_bf16 v[48:51], v[192:195], v[200:203], v[48:51]
	v_mfma_f32_16x16x32_bf16 v[28:31], v[184:187], v[208:211], v[28:31]
	v_mfma_f32_16x16x32_bf16 v[24:27], v[192:195], v[208:211], v[24:27]
	v_mfma_f32_16x16x32_bf16 v[40:43], v[184:187], v[216:219], v[40:43]
	v_mfma_f32_16x16x32_bf16 v[32:35], v[192:195], v[216:219], v[32:35]
	v_mfma_f32_16x16x32_bf16 v[16:19], v[184:187], v[224:227], v[16:19]
	v_mfma_f32_16x16x32_bf16 v[12:15], v[192:195], v[224:227], v[12:15]
	s_setprio 0
	s_add_i32 s39, s39, 2
	s_add_u32 s8, s8, 0x100
	s_addc_u32 s9, s9, 0
	s_cmp_gt_u32 s39, 29
	s_barrier
	s_cbranch_scc0 .LBB0_2750
	s_and_b64 vcc, exec, s[34:35]
	s_cbranch_vccz .LBB0_2753
	s_barrier
